# rows1 row loads batched (were 8 serialized round trips per row), final-norm gain loads prefetched, on top of prefix/krope/epilogue edits
# speedup vs baseline: 1.0316x; 1.0039x over previous
; DEVI float bflo(unsigned w) { return __uint_as_float(w << 16); }
; DEVI float bfhi(unsigned w) { return __uint_as_float(w & 0xffff0000u); }
; template <int MODE>
; DEVI void phase_rows(const Params& p, int l, char* smem) {
;     ...
;         } else { const bf16_t* src = xres + (size_t)row * DM;
; #pragma unroll
;             for (int i = 0; i < 8; ++i) { const u32x2 t = *(const u32x2*)(src + i * 256 + lane * 4); v[i * 4] = bflo(t[0]); v[i * 4 + 1] = bfhi(t[0]); v[i * 4 + 2] = bflo(t[1]); v[i * 4 + 3] = bfhi(t[1]); }
;         }
;     ...
;         if (MODE != 3) { const float* mr2 = (MODE == 2) ? mrow + (size_t)5 * 12288 : mrow;
;             const float* sh = mr2 + ((MODE == 1) ? 6144 : 0); const float* sc = mr2 + ((MODE == 1) ? 8192 : 2048);
; #pragma unroll
;             for (int i = 0; i < 8; ++i) { shv[i] = *(const f32x4*)(sh + i * 256 + lane * 4); scv[i] = *(const f32x4*)(sc + i * 256 + lane * 4); } }
;         float ss = 0.f;
; #pragma unroll
;         for (int i = 0; i < 32; ++i) ss += v[i] * v[i];
;         ss = wave_sum(ss);
;         const float rstd = rsqrtf(ss * (1.f / DM) + EPS);
.LBB0_1043:
	v_ashrrev_i32_e32 v69, 31, v68
	v_lshlrev_b64 v[4:5], 12, v[68:69]
	v_lshl_add_u64 v[4:5], v[70:71], 0, v[4:5]
	s_waitcnt lgkmcnt(0)
	global_load_dwordx2 v[6:7], v[4:5], off
	global_load_dwordx2 v[78:79], v[4:5], off offset:3584
	global_load_dwordx2 v[198:199], v[4:5], off offset:512
	global_load_dwordx2 v[200:201], v[4:5], off offset:1024
	global_load_dwordx2 v[202:203], v[4:5], off offset:1536
	global_load_dwordx2 v[204:205], v[4:5], off offset:2048
	global_load_dwordx2 v[206:207], v[4:5], off offset:2560
	global_load_dwordx2 v[208:209], v[4:5], off offset:3072
	v_cmp_gt_i32_e32 vcc, s90, v68
	v_ashrrev_i32_e32 v151, 11, v68
	v_readlane_b32 s4, v254, 61
	v_readlane_b32 s5, v254, 62
	s_mul_i32 s4, s4, 5
	v_lshlrev_b64 v[80:81], 11, v[68:69]
	v_lshl_add_u64 v[80:81], v[72:73], 0, v[80:81]
	s_waitcnt vmcnt(7)
	v_lshlrev_b32_e32 v179, 16, v6
	v_and_b32_e32 v178, 0xffff0000, v6
	v_lshlrev_b32_e32 v177, 16, v7
	v_and_b32_e32 v176, 0xffff0000, v7
	v_mul_f32_e32 v175, v178, v178
	v_fmac_f32_e32 v175, v179, v179
	v_fmac_f32_e32 v175, v177, v177
	v_fmac_f32_e32 v175, v176, v176
	s_waitcnt vmcnt(6)
	v_and_b32_e32 v76, 0xffff0000, v78
	v_lshlrev_b32_e32 v77, 16, v78
	v_pk_mul_f32 v[180:181], v[76:77], v[76:77]
	s_waitcnt vmcnt(5)
	v_mov_b64_e32 v[6:7], v[198:199]
	v_lshlrev_b32_e32 v174, 16, v6
	v_and_b32_e32 v173, 0xffff0000, v6
	v_lshlrev_b32_e32 v172, 16, v7
	v_and_b32_e32 v171, 0xffff0000, v7
	v_fmac_f32_e32 v175, v174, v174
	v_fmac_f32_e32 v175, v173, v173
	v_fmac_f32_e32 v175, v172, v172
	v_fmac_f32_e32 v175, v171, v171
	s_waitcnt vmcnt(4)
	v_mov_b64_e32 v[6:7], v[200:201]
	v_lshlrev_b32_e32 v170, 16, v6
	v_and_b32_e32 v169, 0xffff0000, v6
	v_lshlrev_b32_e32 v168, 16, v7
	v_and_b32_e32 v167, 0xffff0000, v7
	v_fmac_f32_e32 v175, v170, v170
	v_fmac_f32_e32 v175, v169, v169
	v_fmac_f32_e32 v175, v168, v168
	v_fmac_f32_e32 v175, v167, v167
	s_waitcnt vmcnt(3)
	v_mov_b64_e32 v[6:7], v[202:203]
	v_lshlrev_b32_e32 v166, 16, v6
	v_and_b32_e32 v165, 0xffff0000, v6
	v_lshlrev_b32_e32 v164, 16, v7
	v_and_b32_e32 v163, 0xffff0000, v7
	v_fmac_f32_e32 v175, v166, v166
	v_fmac_f32_e32 v175, v165, v165
	v_fmac_f32_e32 v175, v164, v164
	v_fmac_f32_e32 v175, v163, v163
	s_waitcnt vmcnt(2)
	v_mov_b64_e32 v[6:7], v[204:205]
	v_lshlrev_b32_e32 v162, 16, v6
	v_and_b32_e32 v161, 0xffff0000, v6
	v_lshlrev_b32_e32 v160, 16, v7
	v_and_b32_e32 v159, 0xffff0000, v7
	v_fmac_f32_e32 v175, v162, v162
	v_fmac_f32_e32 v175, v161, v161
	v_fmac_f32_e32 v175, v160, v160
	v_fmac_f32_e32 v175, v159, v159
	s_waitcnt vmcnt(1)
	v_mov_b64_e32 v[6:7], v[206:207]
	v_lshlrev_b32_e32 v158, 16, v6
	v_and_b32_e32 v157, 0xffff0000, v6
	v_lshlrev_b32_e32 v156, 16, v7
	v_and_b32_e32 v155, 0xffff0000, v7
	v_cndmask_b32_e32 v4, 4, v151, vcc
	v_add_u32_e32 v4, s4, v4
	v_readlane_b32 s4, v254, 18
	v_mul_hi_i32_i24_e32 v5, 0xc000, v4
	v_mul_i32_i24_e32 v4, 0xc000, v4
	v_readlane_b32 s5, v254, 19
	v_fmac_f32_e32 v175, v158, v158
	v_fmac_f32_e32 v175, v157, v157
	v_lshl_add_u64 v[4:5], s[4:5], 0, v[4:5]
	v_lshl_add_u64 v[4:5], v[4:5], 0, v[2:3]
	s_mov_b64 s[4:5], 0x6000
	v_lshl_add_u64 v[8:9], v[4:5], 0, s[74:75]
	v_fmac_f32_e32 v175, v156, v156
	v_fmac_f32_e32 v175, v155, v155
	s_waitcnt vmcnt(0)
	v_mov_b64_e32 v[6:7], v[208:209]
	v_lshlrev_b32_e32 v154, 16, v6
	v_and_b32_e32 v153, 0xffff0000, v6
	v_lshlrev_b32_e32 v152, 16, v7
	v_and_b32_e32 v69, 0xffff0000, v7
	v_lshl_add_u64 v[6:7], v[4:5], 0, s[4:5]
	s_movk_i32 s4, 0x7000
	v_add_co_u32_e64 v36, s[50:51], s4, v4
	s_mov_b32 s4, 0x9000
	s_nop 0
	v_addc_co_u32_e64 v37, s[50:51], 0, v5, s[50:51]
	global_load_dwordx4 v[20:23], v[36:37], off offset:-4096
	v_add_co_u32_e64 v38, s[50:51], s4, v4
	v_fmac_f32_e32 v175, v154, v154
	s_nop 0
	v_addc_co_u32_e64 v39, s[50:51], 0, v5, s[50:51]
	global_load_dwordx4 v[64:67], v[38:39], off offset:-4096
	global_load_dwordx4 v[28:31], v[6:7], off offset:1024
	global_load_dwordx4 v[60:63], v[8:9], off offset:1024
	global_load_dwordx4 v[32:35], v[6:7], off offset:2048
	global_load_dwordx4 v[56:59], v[8:9], off offset:2048
	global_load_dwordx4 v[24:27], v[6:7], off offset:3072
	global_load_dwordx4 v[52:55], v[8:9], off offset:3072
	global_load_dwordx4 v[16:19], v[36:37], off
	global_load_dwordx4 v[48:51], v[38:39], off
	global_load_dwordx4 v[12:15], v[36:37], off offset:1024
	global_load_dwordx4 v[44:47], v[38:39], off offset:1024
	s_nop 0
	global_load_dwordx4 v[8:11], v[36:37], off offset:2048
	global_load_dwordx4 v[40:43], v[38:39], off offset:2048
	global_load_dwordx4 v[4:7], v[36:37], off offset:3072
	s_nop 0
	global_load_dwordx4 v[36:39], v[38:39], off offset:3072
	v_fmac_f32_e32 v175, v153, v153
	v_fmac_f32_e32 v175, v152, v152
	v_fmac_f32_e32 v175, v69, v69
	v_add_f32_e32 v78, v181, v175
	v_add_f32_e32 v175, v180, v78
	v_and_b32_e32 v78, 0xffff0000, v79
	v_lshlrev_b32_e32 v79, 16, v79
	v_pk_mul_f32 v[180:181], v[78:79], v[78:79]
	s_waitcnt vmcnt(14)
	v_add_f32_e32 v64, 1.0, v64
	v_add_f32_e32 v175, v181, v175
	v_add_f32_e32 v175, v180, v175
	ds_bpermute_b32 v180, v1, v175
	v_add_f32_e32 v65, 1.0, v65
	s_waitcnt vmcnt(12)
	v_add_f32_e32 v60, 1.0, v60
	s_waitcnt vmcnt(10)
	v_add_f32_e32 v56, 1.0, v56
	s_waitcnt vmcnt(8)
	v_add_f32_e32 v52, 1.0, v52
	s_waitcnt lgkmcnt(0)
	v_add_f32_e32 v175, v175, v180
	ds_bpermute_b32 v180, v75, v175
	s_waitcnt vmcnt(6)
	v_add_f32_e32 v48, 1.0, v48
	s_waitcnt vmcnt(4)
	v_add_f32_e32 v44, 1.0, v44
	s_waitcnt vmcnt(2)
	v_add_f32_e32 v40, 1.0, v40
	s_waitcnt lgkmcnt(0)
	v_add_f32_e32 v175, v175, v180
	ds_bpermute_b32 v180, v82, v175
	s_waitcnt vmcnt(0)
	v_add_f32_e32 v36, 1.0, v36
	s_waitcnt lgkmcnt(0)
	v_add_f32_e32 v175, v175, v180
	ds_bpermute_b32 v180, v83, v175
	s_waitcnt lgkmcnt(0)
; DEVI unsigned cvt_pk(float lo, float hi) { f32x2 v = {lo, hi}; bf16x2_t b = __builtin_convertvector(v, bf16x2_t); return __builtin_bit_cast(unsigned, b); }
; DEVI unsigned cvt4_fp8c(float a, float b, float c, float d) { return cvt4_fp8(clamp8(a), clamp8(b), clamp8(c), clamp8(d)); }
; template <int MODE>
; DEVI void phase_rows(const Params& p, int l, char* smem) {
;     ...
;         ss = wave_sum(ss);
;         const float rstd = rsqrtf(ss * (1.f / DM) + EPS);
;         if (MODE == 3) {
; #pragma unroll
;             for (int i = 0; i < 8; ++i) { const f32x4 g = *(const f32x4*)(p.final_norm + i * 256 + lane * 4);
;                 __builtin_nontemporal_store((f32x4){v[i * 4] * rstd * g[0], v[i * 4 + 1] * rstd * g[1], v[i * 4 + 2] * rstd * g[2], v[i * 4 + 3] * rstd * g[3]}, (f32x4*)(p.out + (size_t)row * DM + i * 256 + lane * 4)); }
;             continue;
;         }
; #pragma unroll
;         for (int i = 0; i < 8; ++i) { const f32x4 a = shv[i]; const f32x4 s = scv[i];
; #pragma unroll
;             for (int j = 0; j < 4; ++j) v[i * 4 + j] = v[i * 4 + j] * rstd * (1.f + s[j]) + a[j];
;             if (MODE == 1) *(unsigned*)((unsigned char*)hbuf + (size_t)row * DM + i * 256 + lane * 4) = cvt4_fp8c(v[i * 4], v[i * 4 + 1], v[i * 4 + 2], v[i * 4 + 3]);
;             else *(u32x2*)(hbuf + (size_t)row * DM + i * 256 + lane * 4) = (u32x2){cvt_pk(v[i * 4], v[i * 4 + 1]), cvt_pk(v[i * 4 + 2], v[i * 4 + 3])}; }
;         if (MODE == 1) {
;             float a[16];
; #pragma unroll
;             for (int e = 0; e < 16; ++e) { float t = 0.f;
; #pragma unroll
;                 for (int i = 0; i < 8; ++i) { const f32x4 w = *(const f32x4*)(wT + e * 2048 + i * 256 + lane * 4);
;                     t += v[i * 4] * w[0] + v[i * 4 + 1] * w[1] + v[i * 4 + 2] * w[2] + v[i * 4 + 3] * w[3]; }
;                 a[e] = t; if ((e & 3) == 3) __builtin_amdgcn_sched_barrier(0); }
	v_add_f32_e32 v175, v175, v180
	ds_bpermute_b32 v180, v84, v175
	s_waitcnt lgkmcnt(0)
	v_add_f32_e32 v175, v175, v180
	ds_bpermute_b32 v180, v85, v175
	s_waitcnt lgkmcnt(0)
	v_add_f32_e32 v175, v175, v180
	v_fmamk_f32 v175, v175, 0x3a000000, v223
	v_cmp_gt_f32_e64 s[50:51], s97, v175
	v_mul_f32_e32 v180, 0x4b800000, v175
	s_nop 0
	v_cndmask_b32_e64 v175, v175, v180, s[50:51]
	v_rsq_f32_e32 v175, v175
	s_nop 0
	v_mul_f32_e32 v180, 0x45800000, v175
	v_cndmask_b32_e64 v175, v175, v180, s[50:51]
	v_mul_f32_e32 v179, v175, v179
	v_fma_f32 v20, v64, v179, v20
	v_mul_f32_e32 v64, v175, v178
	v_fma_f32 v64, v65, v64, v21
	v_mul_f32_e32 v21, v175, v177
	v_add_f32_e32 v65, 1.0, v66
	v_fma_f32 v21, v65, v21, v22
	v_mul_f32_e32 v22, v175, v176
	v_add_f32_e32 v65, 1.0, v67
	v_fmac_f32_e32 v23, v65, v22
	v_med3_f32 v22, v20, s89, v238
	v_med3_f32 v65, v64, s89, v238
	v_mov_b32_e32 v176, v3
	v_cvt_pk_fp8_f32 v176, v22, v65
	v_mul_f32_e32 v22, v175, v174
	v_fma_f32 v22, v60, v22, v28
	v_mul_f32_e32 v28, v175, v173
	v_add_f32_e32 v60, 1.0, v61
	v_fma_f32 v29, v60, v28, v29
	v_mul_f32_e32 v28, v175, v172
	v_add_f32_e32 v60, 1.0, v62
	v_fma_f32 v28, v60, v28, v30
	v_mul_f32_e32 v30, v175, v171
	v_add_f32_e32 v60, 1.0, v63
	v_fmac_f32_e32 v31, v60, v30
	v_med3_f32 v30, v22, s89, v238
	v_med3_f32 v60, v29, s89, v238
	v_mov_b32_e32 v63, v3
	v_cvt_pk_fp8_f32 v63, v30, v60
	v_mul_f32_e32 v30, v175, v170
	v_fma_f32 v30, v56, v30, v32
	v_mul_f32_e32 v32, v175, v169
	v_add_f32_e32 v56, 1.0, v57
	v_fma_f32 v33, v56, v32, v33
	v_mul_f32_e32 v32, v175, v168
	v_add_f32_e32 v56, 1.0, v58
	v_fma_f32 v32, v56, v32, v34
	v_mul_f32_e32 v34, v175, v167
	v_add_f32_e32 v56, 1.0, v59
	v_fmac_f32_e32 v35, v56, v34
	v_med3_f32 v34, v30, s89, v238
	v_med3_f32 v56, v33, s89, v238
	v_mov_b32_e32 v59, v3
	v_cvt_pk_fp8_f32 v59, v34, v56
	v_mul_f32_e32 v34, v175, v166
	v_fma_f32 v24, v52, v34, v24
	v_mul_f32_e32 v34, v175, v165
	v_add_f32_e32 v52, 1.0, v53
	v_fma_f32 v34, v52, v34, v25
	v_mul_f32_e32 v25, v175, v164
	v_add_f32_e32 v52, 1.0, v54
	v_fma_f32 v25, v52, v25, v26
	v_mul_f32_e32 v26, v175, v163
	v_add_f32_e32 v52, 1.0, v55
	v_fmac_f32_e32 v27, v52, v26
	v_med3_f32 v26, v24, s89, v238
	v_med3_f32 v52, v34, s89, v238
	v_mov_b32_e32 v55, v3
	v_cvt_pk_fp8_f32 v55, v26, v52
	v_mul_f32_e32 v26, v175, v162
	v_fma_f32 v16, v48, v26, v16
	v_mul_f32_e32 v26, v175, v161
	v_add_f32_e32 v48, 1.0, v49
	v_fma_f32 v26, v48, v26, v17
	v_mul_f32_e32 v17, v175, v160
	v_add_f32_e32 v48, 1.0, v50
	v_fma_f32 v17, v48, v17, v18
	v_mul_f32_e32 v18, v175, v159
	v_add_f32_e32 v48, 1.0, v51
	v_fmac_f32_e32 v19, v48, v18
	v_med3_f32 v18, v16, s89, v238
	v_med3_f32 v48, v26, s89, v238
	v_mov_b32_e32 v51, v3
	v_cvt_pk_fp8_f32 v51, v18, v48
	v_mul_f32_e32 v18, v175, v158
	v_fma_f32 v12, v44, v18, v12
	v_mul_f32_e32 v18, v175, v157
	v_add_f32_e32 v44, 1.0, v45
	v_fma_f32 v18, v44, v18, v13
	v_mul_f32_e32 v13, v175, v156
	v_add_f32_e32 v44, 1.0, v46
	v_fma_f32 v13, v44, v13, v14
	v_mul_f32_e32 v14, v175, v155
	v_add_f32_e32 v44, 1.0, v47
	v_fmac_f32_e32 v15, v44, v14
	v_med3_f32 v14, v12, s89, v238
	v_med3_f32 v44, v18, s89, v238
	v_mov_b32_e32 v47, v3
	v_cvt_pk_fp8_f32 v47, v14, v44
	v_mul_f32_e32 v14, v175, v154
	v_fma_f32 v8, v40, v14, v8
	v_mul_f32_e32 v14, v175, v153
	v_add_f32_e32 v40, 1.0, v41
	v_fma_f32 v14, v40, v14, v9
	v_mul_f32_e32 v9, v175, v152
	v_add_f32_e32 v40, 1.0, v42
	v_fma_f32 v9, v40, v9, v10
	v_mul_f32_e32 v10, v175, v69
	v_add_f32_e32 v40, 1.0, v43
	v_fmac_f32_e32 v11, v40, v10
	v_med3_f32 v10, v8, s89, v238
	v_med3_f32 v40, v14, s89, v238
	v_mov_b32_e32 v43, v3
	v_cvt_pk_fp8_f32 v43, v10, v40
	v_mul_f32_e32 v10, v175, v77
	v_fma_f32 v4, v36, v10, v4
	v_mul_f32_e32 v10, v175, v76
	v_add_f32_e32 v36, 1.0, v37
	v_fma_f32 v10, v36, v10, v5
	v_mul_f32_e32 v5, v175, v79
	v_add_f32_e32 v36, 1.0, v38
	v_fma_f32 v5, v36, v5, v6
	v_mul_f32_e32 v6, v175, v78
	v_add_f32_e32 v36, 1.0, v39
	v_fmac_f32_e32 v7, v36, v6
	v_med3_f32 v6, v4, s89, v238
	v_med3_f32 v36, v10, s89, v238
	v_mov_b32_e32 v39, v3
	v_cvt_pk_fp8_f32 v39, v6, v36
	v_med3_f32 v37, v5, s89, v238
	v_med3_f32 v38, v7, s89, v238
	v_med3_f32 v66, v21, s89, v238
	v_cvt_pk_fp8_f32 v39, v37, v38 op_sel:[0,0,1]
	v_med3_f32 v67, v23, s89, v238
	v_med3_f32 v61, v28, s89, v238
	v_med3_f32 v62, v31, s89, v238
	global_store_dword v[80:81], v39, off offset:1792
	ds_read_b128 v[36:39], v86
	v_med3_f32 v57, v32, s89, v238
	v_med3_f32 v58, v35, s89, v238
	v_med3_f32 v53, v25, s89, v238
	v_med3_f32 v54, v27, s89, v238
	s_waitcnt lgkmcnt(0)
	v_mul_f32_e32 v6, v64, v37
	v_fmac_f32_e32 v6, v20, v36
	v_fmac_f32_e32 v6, v21, v38
	v_fmac_f32_e32 v6, v23, v39
	ds_read_b128 v[36:39], v86 offset:1024
	v_add_f32_e32 v6, 0, v6
	v_med3_f32 v49, v17, s89, v238
	v_med3_f32 v50, v19, s89, v238
	v_med3_f32 v45, v13, s89, v238
	s_waitcnt lgkmcnt(0)
	v_mul_f32_e32 v37, v29, v37
	v_fmac_f32_e32 v37, v22, v36
	v_fmac_f32_e32 v37, v28, v38
	v_fmac_f32_e32 v37, v31, v39
	v_add_f32_e32 v6, v6, v37
	ds_read_b128 v[36:39], v86 offset:2048
	v_med3_f32 v46, v15, s89, v238
	v_med3_f32 v41, v9, s89, v238
	v_med3_f32 v42, v11, s89, v238
	v_cvt_pk_fp8_f32 v176, v66, v67 op_sel:[0,0,1]
	s_waitcnt lgkmcnt(0)
	v_mul_f32_e32 v37, v33, v37
	v_fmac_f32_e32 v37, v30, v36
	v_fmac_f32_e32 v37, v32, v38
	v_fmac_f32_e32 v37, v35, v39
	v_add_f32_e32 v6, v6, v37
	ds_read_b128 v[36:39], v86 offset:3072
	v_cvt_pk_fp8_f32 v63, v61, v62 op_sel:[0,0,1]
	v_cvt_pk_fp8_f32 v59, v57, v58 op_sel:[0,0,1]
	v_cvt_pk_fp8_f32 v55, v53, v54 op_sel:[0,0,1]
	v_cvt_pk_fp8_f32 v51, v49, v50 op_sel:[0,0,1]
	s_waitcnt lgkmcnt(0)
; DEVI unsigned cvt_pk(float lo, float hi) { f32x2 v = {lo, hi}; bf16x2_t b = __builtin_convertvector(v, bf16x2_t); return __builtin_bit_cast(unsigned, b); }
; DEVI unsigned cvt4_fp8c(float a, float b, float c, float d) { return cvt4_fp8(clamp8(a), clamp8(b), clamp8(c), clamp8(d)); }
; template <int MODE>
; DEVI void phase_rows(const Params& p, int l, char* smem) {
;     ...
;             if (MODE == 1) *(unsigned*)((unsigned char*)hbuf + (size_t)row * DM + i * 256 + lane * 4) = cvt4_fp8c(v[i * 4], v[i * 4 + 1], v[i * 4 + 2], v[i * 4 + 3]);
;             else *(u32x2*)(hbuf + (size_t)row * DM + i * 256 + lane * 4) = (u32x2){cvt_pk(v[i * 4], v[i * 4 + 1]), cvt_pk(v[i * 4 + 2], v[i * 4 + 3])}; }
;         if (MODE == 1) {
;             float a[16];
; #pragma unroll
;             for (int e = 0; e < 16; ++e) { float t = 0.f;
; #pragma unroll
;                 for (int i = 0; i < 8; ++i) { const f32x4 w = *(const f32x4*)(wT + e * 2048 + i * 256 + lane * 4);
;                     t += v[i * 4] * w[0] + v[i * 4 + 1] * w[1] + v[i * 4 + 2] * w[2] + v[i * 4 + 3] * w[3]; }
;                 a[e] = t; if ((e & 3) == 3) __builtin_amdgcn_sched_barrier(0); }
	v_mul_f32_e32 v37, v34, v37
	v_fmac_f32_e32 v37, v24, v36
	v_fmac_f32_e32 v37, v25, v38
	v_fmac_f32_e32 v37, v27, v39
	v_add_f32_e32 v6, v6, v37
	ds_read_b128 v[36:39], v86 offset:4096
	v_cvt_pk_fp8_f32 v47, v45, v46 op_sel:[0,0,1]
	v_cvt_pk_fp8_f32 v43, v41, v42 op_sel:[0,0,1]
	global_store_dword v[80:81], v176, off
	global_store_dword v[80:81], v63, off offset:256
	s_waitcnt lgkmcnt(0)
	v_mul_f32_e32 v37, v26, v37
	v_fmac_f32_e32 v37, v16, v36
	v_fmac_f32_e32 v37, v17, v38
	v_fmac_f32_e32 v37, v19, v39
	v_add_f32_e32 v6, v6, v37
	ds_read_b128 v[36:39], v86 offset:5120
	global_store_dword v[80:81], v59, off offset:512
	global_store_dword v[80:81], v55, off offset:768
	global_store_dword v[80:81], v51, off offset:1024
	global_store_dword v[80:81], v47, off offset:1280
	s_waitcnt lgkmcnt(0)
	v_mul_f32_e32 v37, v18, v37
	v_fmac_f32_e32 v37, v12, v36
	v_fmac_f32_e32 v37, v13, v38
	v_fmac_f32_e32 v37, v15, v39
	v_add_f32_e32 v6, v6, v37
	ds_read_b128 v[36:39], v86 offset:6144
	global_store_dword v[80:81], v43, off offset:1536
	s_waitcnt lgkmcnt(0)
	v_mul_f32_e32 v37, v14, v37
	v_fmac_f32_e32 v37, v8, v36
	v_fmac_f32_e32 v37, v9, v38
	v_fmac_f32_e32 v37, v11, v39
	v_add_f32_e32 v6, v6, v37
	ds_read_b128 v[36:39], v86 offset:7168
	s_waitcnt lgkmcnt(0)
	v_mul_f32_e32 v37, v10, v37
	v_fmac_f32_e32 v37, v4, v36
	v_fmac_f32_e32 v37, v5, v38
	v_fmac_f32_e32 v37, v7, v39
	v_add_f32_e32 v6, v6, v37
	ds_read_b128 v[36:39], v86 offset:15360
	ds_read_b128 v[40:43], v86 offset:14336
	ds_read_b128 v[44:47], v86 offset:13312
	ds_read_b128 v[48:51], v86 offset:12288
	ds_read_b128 v[52:55], v86 offset:11264
	ds_read_b128 v[56:59], v86 offset:10240
	ds_read_b128 v[60:63], v86 offset:9216
	ds_read_b128 v[76:79], v86 offset:8192
	s_waitcnt lgkmcnt(4)
	v_mul_f32_e32 v49, v26, v49
	s_waitcnt lgkmcnt(3)
	v_mul_f32_e32 v53, v34, v53
	s_waitcnt lgkmcnt(2)
	v_mul_f32_e32 v57, v33, v57
	s_waitcnt lgkmcnt(1)
	v_mul_f32_e32 v61, v29, v61
	s_waitcnt lgkmcnt(0)
	v_mul_f32_e32 v65, v64, v77
	v_fmac_f32_e32 v65, v20, v76
	v_fmac_f32_e32 v65, v21, v78
	v_fmac_f32_e32 v61, v22, v60
	v_fmac_f32_e32 v65, v23, v79
	v_fmac_f32_e32 v61, v28, v62
	v_fmac_f32_e32 v57, v30, v56
	v_add_f32_e32 v65, 0, v65
	v_fmac_f32_e32 v61, v31, v63
	v_fmac_f32_e32 v57, v32, v58
	v_fmac_f32_e32 v53, v24, v52
	v_add_f32_e32 v60, v61, v65
	v_fmac_f32_e32 v57, v35, v59
	v_fmac_f32_e32 v53, v25, v54
	v_fmac_f32_e32 v49, v16, v48
	v_mul_f32_e32 v45, v18, v45
	v_add_f32_e32 v56, v57, v60
	v_fmac_f32_e32 v53, v27, v55
	v_fmac_f32_e32 v49, v17, v50
	v_fmac_f32_e32 v45, v12, v44
	v_mul_f32_e32 v41, v14, v41
	v_add_f32_e32 v52, v53, v56
	v_fmac_f32_e32 v49, v19, v51
	v_fmac_f32_e32 v45, v13, v46
	v_fmac_f32_e32 v41, v8, v40
	v_mul_f32_e32 v37, v10, v37
	v_add_f32_e32 v48, v49, v52
	v_fmac_f32_e32 v45, v15, v47
	v_fmac_f32_e32 v41, v9, v42
	v_fmac_f32_e32 v37, v4, v36
	v_add_f32_e32 v44, v45, v48
	v_fmac_f32_e32 v41, v11, v43
	v_fmac_f32_e32 v37, v5, v38
	v_add_f32_e32 v40, v41, v44
	v_fmac_f32_e32 v37, v7, v39
	v_add_f32_e32 v36, v37, v40
	ds_read_b128 v[38:41], v86 offset:23552
	ds_read_b128 v[42:45], v86 offset:22528
	ds_read_b128 v[46:49], v86 offset:21504
	ds_read_b128 v[50:53], v86 offset:20480
	ds_read_b128 v[54:57], v86 offset:19456
	ds_read_b128 v[58:61], v86 offset:18432
	ds_read_b128 v[76:79], v86 offset:17408
	ds_read_b128 v[152:155], v86 offset:16384
	s_waitcnt lgkmcnt(4)
	v_mul_f32_e32 v51, v26, v51
	s_waitcnt lgkmcnt(3)
	v_mul_f32_e32 v55, v34, v55
	s_waitcnt lgkmcnt(2)
	v_mul_f32_e32 v59, v33, v59
	s_waitcnt lgkmcnt(1)
	v_mul_f32_e32 v62, v29, v77
	s_waitcnt lgkmcnt(0)
	v_mul_f32_e32 v37, v64, v153
	v_fmac_f32_e32 v37, v20, v152
	v_fmac_f32_e32 v37, v21, v154
	v_fmac_f32_e32 v62, v22, v76
	v_fmac_f32_e32 v37, v23, v155
	v_fmac_f32_e32 v62, v28, v78
	v_fmac_f32_e32 v59, v30, v58
	v_add_f32_e32 v37, 0, v37
	v_fmac_f32_e32 v62, v31, v79
	v_fmac_f32_e32 v59, v32, v60
	v_fmac_f32_e32 v55, v24, v54
	v_add_f32_e32 v37, v62, v37
	v_fmac_f32_e32 v59, v35, v61
	v_fmac_f32_e32 v55, v25, v56
	v_fmac_f32_e32 v51, v16, v50
	v_mul_f32_e32 v47, v18, v47
	v_add_f32_e32 v37, v59, v37
	v_fmac_f32_e32 v55, v27, v57
	v_fmac_f32_e32 v51, v17, v52
	v_fmac_f32_e32 v47, v12, v46
	v_mul_f32_e32 v43, v14, v43
	v_add_f32_e32 v37, v55, v37
	v_fmac_f32_e32 v51, v19, v53
	v_fmac_f32_e32 v47, v13, v48
	v_fmac_f32_e32 v43, v8, v42
	v_mul_f32_e32 v39, v10, v39
	v_add_f32_e32 v37, v51, v37
	v_fmac_f32_e32 v47, v15, v49
	v_fmac_f32_e32 v43, v9, v44
	v_fmac_f32_e32 v39, v4, v38
	v_add_f32_e32 v37, v47, v37
	v_fmac_f32_e32 v43, v11, v45
	v_fmac_f32_e32 v39, v5, v40
	v_add_f32_e32 v37, v43, v37
	v_fmac_f32_e32 v39, v7, v41
	v_add_f32_e32 v37, v39, v37
	ds_read_b128 v[38:41], v86 offset:31744
	ds_read_b128 v[42:45], v86 offset:30720
	ds_read_b128 v[46:49], v86 offset:29696
	ds_read_b128 v[50:53], v86 offset:28672
	ds_read_b128 v[54:57], v86 offset:27648
	ds_read_b128 v[58:61], v86 offset:26624
	ds_read_b128 v[76:79], v86 offset:25600
	ds_read_b128 v[152:155], v86 offset:24576
	s_waitcnt lgkmcnt(4)
	v_mul_f32_e32 v51, v26, v51
	s_waitcnt lgkmcnt(3)
	v_mul_f32_e32 v55, v34, v55
	s_waitcnt lgkmcnt(2)
	v_mul_f32_e32 v59, v33, v59
	s_waitcnt lgkmcnt(1)
	v_mul_f32_e32 v63, v29, v77
	s_waitcnt lgkmcnt(0)
; template <int MODE>
; DEVI void phase_rows(const Params& p, int l, char* smem) {
;     ...
;             for (int e = 0; e < 16; ++e) { float t = 0.f;
; #pragma unroll
;                 for (int i = 0; i < 8; ++i) { const f32x4 w = *(const f32x4*)(wT + e * 2048 + i * 256 + lane * 4);
;                     t += v[i * 4] * w[0] + v[i * 4 + 1] * w[1] + v[i * 4 + 2] * w[2] + v[i * 4 + 3] * w[3]; }
;                 a[e] = t; if ((e & 3) == 3) __builtin_amdgcn_sched_barrier(0); }
	v_mul_f32_e32 v62, v64, v153
	v_fmac_f32_e32 v62, v20, v152
	v_fmac_f32_e32 v62, v21, v154
	v_fmac_f32_e32 v63, v22, v76
	v_fmac_f32_e32 v62, v23, v155
	v_fmac_f32_e32 v63, v28, v78
	v_fmac_f32_e32 v59, v30, v58
	v_add_f32_e32 v62, 0, v62
	v_fmac_f32_e32 v63, v31, v79
	v_fmac_f32_e32 v59, v32, v60
	v_fmac_f32_e32 v55, v24, v54
	v_add_f32_e32 v62, v63, v62
	v_fmac_f32_e32 v59, v35, v61
	v_fmac_f32_e32 v55, v25, v56
	v_fmac_f32_e32 v51, v16, v50
	v_mul_f32_e32 v47, v18, v47
	v_add_f32_e32 v58, v59, v62
	v_fmac_f32_e32 v55, v27, v57
	v_fmac_f32_e32 v51, v17, v52
	v_fmac_f32_e32 v47, v12, v46
	v_mul_f32_e32 v43, v14, v43
	v_add_f32_e32 v54, v55, v58
	v_fmac_f32_e32 v51, v19, v53
	v_fmac_f32_e32 v47, v13, v48
	v_fmac_f32_e32 v43, v8, v42
	v_mul_f32_e32 v39, v10, v39
	v_add_f32_e32 v50, v51, v54
	v_fmac_f32_e32 v47, v15, v49
	v_fmac_f32_e32 v43, v9, v44
	v_fmac_f32_e32 v39, v4, v38
	v_add_f32_e32 v46, v47, v50
	v_fmac_f32_e32 v43, v11, v45
	v_fmac_f32_e32 v39, v5, v40
	v_add_f32_e32 v42, v43, v46
	v_fmac_f32_e32 v39, v7, v41
	v_add_f32_e32 v38, v39, v42
	ds_read_b128 v[40:43], v86 offset:32768
	ds_read_b128 v[44:47], v86 offset:33792
	ds_read_b128 v[48:51], v86 offset:34816
	s_waitcnt lgkmcnt(2)
	v_mul_f32_e32 v39, v64, v41
	s_waitcnt lgkmcnt(1)
	v_mul_f32_e32 v41, v29, v45
	v_fmac_f32_e32 v39, v20, v40
	v_fmac_f32_e32 v41, v22, v44
	v_fmac_f32_e32 v39, v21, v42
	v_fmac_f32_e32 v39, v23, v43
	v_fmac_f32_e32 v41, v28, v46
	v_add_f32_e32 v39, 0, v39
	v_fmac_f32_e32 v41, v31, v47
	v_add_f32_e32 v39, v39, v41
	ds_read_b128 v[40:43], v86 offset:35840
	s_waitcnt lgkmcnt(1)
	v_mul_f32_e32 v44, v33, v49
	v_fmac_f32_e32 v44, v30, v48
	v_fmac_f32_e32 v44, v32, v50
	v_fmac_f32_e32 v44, v35, v51
	v_add_f32_e32 v39, v39, v44
	ds_read_b128 v[44:47], v86 offset:36864
	s_waitcnt lgkmcnt(1)
	v_mul_f32_e32 v41, v34, v41
	v_fmac_f32_e32 v41, v24, v40
	v_fmac_f32_e32 v41, v25, v42
	v_fmac_f32_e32 v41, v27, v43
	v_add_f32_e32 v39, v39, v41
	ds_read_b128 v[40:43], v86 offset:37888
	s_waitcnt lgkmcnt(1)
	v_mul_f32_e32 v45, v26, v45
	v_fmac_f32_e32 v45, v16, v44
	v_fmac_f32_e32 v45, v17, v46
	v_fmac_f32_e32 v45, v19, v47
	v_add_f32_e32 v39, v39, v45
	ds_read_b128 v[44:47], v86 offset:38912
	s_waitcnt lgkmcnt(1)
	v_mul_f32_e32 v41, v18, v41
	v_fmac_f32_e32 v41, v12, v40
	v_fmac_f32_e32 v41, v13, v42
	v_fmac_f32_e32 v41, v15, v43
	v_add_f32_e32 v39, v39, v41
	ds_read_b128 v[40:43], v86 offset:39936
	s_waitcnt lgkmcnt(1)
	v_mul_f32_e32 v45, v14, v45
	v_fmac_f32_e32 v45, v8, v44
	v_fmac_f32_e32 v45, v9, v46
	v_fmac_f32_e32 v45, v11, v47
	s_waitcnt lgkmcnt(0)
	v_mul_f32_e32 v41, v10, v41
	v_fmac_f32_e32 v41, v4, v40
	v_fmac_f32_e32 v41, v5, v42
	v_add_f32_e32 v39, v39, v45
	v_fmac_f32_e32 v41, v7, v43
	v_add_f32_e32 v39, v39, v41
	ds_read_b128 v[40:43], v86 offset:48128
	ds_read_b128 v[44:47], v86 offset:47104
	ds_read_b128 v[48:51], v86 offset:41984
	ds_read_b128 v[52:55], v86 offset:40960
	ds_read_b128 v[56:59], v86 offset:46080
	ds_read_b128 v[60:63], v86 offset:45056
	ds_read_b128 v[76:79], v86 offset:44032
	ds_read_b128 v[152:155], v86 offset:43008
	s_waitcnt lgkmcnt(4)
	v_mul_f32_e32 v53, v64, v53
	v_fmac_f32_e32 v53, v20, v52
	v_mul_f32_e32 v49, v29, v49
	v_fmac_f32_e32 v53, v21, v54
	v_fmac_f32_e32 v49, v22, v48
	v_fmac_f32_e32 v53, v23, v55
	v_fmac_f32_e32 v49, v28, v50
	v_add_f32_e32 v52, 0, v53
	v_fmac_f32_e32 v49, v31, v51
	v_add_f32_e32 v48, v49, v52
	s_waitcnt lgkmcnt(0)
	v_mul_f32_e32 v49, v33, v153
	v_fmac_f32_e32 v49, v30, v152
	v_fmac_f32_e32 v49, v32, v154
	v_fmac_f32_e32 v49, v35, v155
	v_add_f32_e32 v48, v49, v48
	v_mul_f32_e32 v49, v34, v77
	v_fmac_f32_e32 v49, v24, v76
	v_fmac_f32_e32 v49, v25, v78
	v_fmac_f32_e32 v49, v27, v79
	v_add_f32_e32 v48, v49, v48
	v_mul_f32_e32 v49, v26, v61
	v_fmac_f32_e32 v49, v16, v60
	v_fmac_f32_e32 v49, v17, v62
	v_fmac_f32_e32 v49, v19, v63
	v_add_f32_e32 v48, v49, v48
	v_mul_f32_e32 v49, v18, v57
	v_fmac_f32_e32 v49, v12, v56
	v_mul_f32_e32 v45, v14, v45
	v_fmac_f32_e32 v49, v13, v58
	v_fmac_f32_e32 v45, v8, v44
	v_mul_f32_e32 v41, v10, v41
	v_fmac_f32_e32 v49, v15, v59
	v_fmac_f32_e32 v45, v9, v46
	v_fmac_f32_e32 v41, v4, v40
	v_add_f32_e32 v48, v49, v48
	v_fmac_f32_e32 v45, v11, v47
	v_fmac_f32_e32 v41, v5, v42
	v_add_f32_e32 v44, v45, v48
	v_fmac_f32_e32 v41, v7, v43
	v_add_f32_e32 v40, v41, v44
	ds_read_b128 v[42:45], v86 offset:56320
	ds_read_b128 v[46:49], v86 offset:55296
	ds_read_b128 v[50:53], v86 offset:50176
	ds_read_b128 v[54:57], v86 offset:49152
	ds_read_b128 v[58:61], v86 offset:54272
	ds_read_b128 v[76:79], v86 offset:53248
	ds_read_b128 v[152:155], v86 offset:52224
	ds_read_b128 v[156:159], v86 offset:51200
	s_waitcnt lgkmcnt(4)
	v_mul_f32_e32 v41, v64, v55
	v_fmac_f32_e32 v41, v20, v54
	v_mul_f32_e32 v51, v29, v51
	v_fmac_f32_e32 v41, v21, v56
	v_fmac_f32_e32 v51, v22, v50
	s_waitcnt lgkmcnt(0)
	v_mul_f32_e32 v50, v33, v157
	v_fmac_f32_e32 v41, v23, v57
	v_fmac_f32_e32 v51, v28, v52
	v_fmac_f32_e32 v50, v30, v156
	v_add_f32_e32 v41, 0, v41
	v_fmac_f32_e32 v51, v31, v53
	v_fmac_f32_e32 v50, v32, v158
	v_add_f32_e32 v41, v51, v41
	v_fmac_f32_e32 v50, v35, v159
	v_add_f32_e32 v41, v50, v41
	v_mul_f32_e32 v50, v34, v153
	v_fmac_f32_e32 v50, v24, v152
	v_fmac_f32_e32 v50, v25, v154
	v_fmac_f32_e32 v50, v27, v155
	v_add_f32_e32 v41, v50, v41
	v_mul_f32_e32 v50, v26, v77
	v_fmac_f32_e32 v50, v16, v76
	v_fmac_f32_e32 v50, v17, v78
	v_fmac_f32_e32 v50, v19, v79
	v_add_f32_e32 v41, v50, v41
	v_mul_f32_e32 v50, v18, v59
	v_fmac_f32_e32 v50, v12, v58
	v_mul_f32_e32 v47, v14, v47
	v_fmac_f32_e32 v50, v13, v60
	v_fmac_f32_e32 v47, v8, v46
	v_mul_f32_e32 v43, v10, v43
	v_fmac_f32_e32 v50, v15, v61
	v_fmac_f32_e32 v47, v9, v48
	v_fmac_f32_e32 v43, v4, v42
	v_add_f32_e32 v41, v50, v41
	v_fmac_f32_e32 v47, v11, v49
	v_fmac_f32_e32 v43, v5, v44
	v_add_f32_e32 v41, v47, v41
	v_fmac_f32_e32 v43, v7, v45
	v_add_f32_e32 v41, v43, v41
	ds_read_b128 v[42:45], v86 offset:64512
	ds_read_b128 v[46:49], v86 offset:63488
	ds_read_b128 v[50:53], v86 offset:58368
	ds_read_b128 v[54:57], v86 offset:57344
	ds_read_b128 v[58:61], v86 offset:62464
	ds_read_b128 v[76:79], v86 offset:61440
	ds_read_b128 v[152:155], v86 offset:60416
	ds_read_b128 v[156:159], v86 offset:59392
	s_waitcnt lgkmcnt(4)
; template <int MODE>
; DEVI void phase_rows(const Params& p, int l, char* smem) {
;     ...
;             for (int e = 0; e < 16; ++e) { float t = 0.f;
; #pragma unroll
;                 for (int i = 0; i < 8; ++i) { const f32x4 w = *(const f32x4*)(wT + e * 2048 + i * 256 + lane * 4);
;                     t += v[i * 4] * w[0] + v[i * 4 + 1] * w[1] + v[i * 4 + 2] * w[2] + v[i * 4 + 3] * w[3]; }
;                 a[e] = t; if ((e & 3) == 3) __builtin_amdgcn_sched_barrier(0); }
	v_mul_f32_e32 v55, v64, v55
	v_fmac_f32_e32 v55, v20, v54
	v_mul_f32_e32 v51, v29, v51
	v_fmac_f32_e32 v55, v21, v56
	v_fmac_f32_e32 v51, v22, v50
	v_fmac_f32_e32 v55, v23, v57
	v_fmac_f32_e32 v51, v28, v52
	v_add_f32_e32 v54, 0, v55
	v_fmac_f32_e32 v51, v31, v53
	v_add_f32_e32 v50, v51, v54
	s_waitcnt lgkmcnt(0)
	v_mul_f32_e32 v51, v33, v157
	v_fmac_f32_e32 v51, v30, v156
	v_fmac_f32_e32 v51, v32, v158
	v_fmac_f32_e32 v51, v35, v159
	v_add_f32_e32 v50, v51, v50
	v_mul_f32_e32 v51, v34, v153
	v_fmac_f32_e32 v51, v24, v152
	v_fmac_f32_e32 v51, v25, v154
	v_fmac_f32_e32 v51, v27, v155
	v_add_f32_e32 v50, v51, v50
	v_mul_f32_e32 v51, v26, v77
	v_fmac_f32_e32 v51, v16, v76
	v_fmac_f32_e32 v51, v17, v78
	v_fmac_f32_e32 v51, v19, v79
	v_add_f32_e32 v50, v51, v50
	v_mul_f32_e32 v51, v18, v59
	v_fmac_f32_e32 v51, v12, v58
	v_mul_f32_e32 v47, v14, v47
	v_fmac_f32_e32 v51, v13, v60
	v_fmac_f32_e32 v47, v8, v46
	v_mul_f32_e32 v43, v10, v43
	v_fmac_f32_e32 v51, v15, v61
	v_fmac_f32_e32 v47, v9, v48
	v_fmac_f32_e32 v43, v4, v42
	v_add_f32_e32 v50, v51, v50
	v_fmac_f32_e32 v47, v11, v49
	v_fmac_f32_e32 v43, v5, v44
	v_add_f32_e32 v46, v47, v50
	v_fmac_f32_e32 v43, v7, v45
	v_add_f32_e32 v42, v43, v46
	ds_read_b128 v[44:47], v87
	ds_read_b128 v[48:51], v88
	ds_read_b128 v[52:55], v89
	s_waitcnt lgkmcnt(2)
	v_mul_f32_e32 v43, v64, v45
	s_waitcnt lgkmcnt(1)
	v_mul_f32_e32 v45, v29, v49
	v_fmac_f32_e32 v43, v20, v44
	v_fmac_f32_e32 v45, v22, v48
	v_fmac_f32_e32 v43, v21, v46
	v_fmac_f32_e32 v43, v23, v47
	v_fmac_f32_e32 v45, v28, v50
	v_add_f32_e32 v43, 0, v43
	v_fmac_f32_e32 v45, v31, v51
	v_add_f32_e32 v43, v43, v45
	ds_read_b128 v[44:47], v90
	s_waitcnt lgkmcnt(1)
	v_mul_f32_e32 v48, v33, v53
	v_fmac_f32_e32 v48, v30, v52
	v_fmac_f32_e32 v48, v32, v54
	v_fmac_f32_e32 v48, v35, v55
	v_add_f32_e32 v43, v43, v48
	ds_read_b128 v[48:51], v91
	s_waitcnt lgkmcnt(1)
	v_mul_f32_e32 v45, v34, v45
	v_fmac_f32_e32 v45, v24, v44
	v_fmac_f32_e32 v45, v25, v46
	v_fmac_f32_e32 v45, v27, v47
	v_add_f32_e32 v43, v43, v45
	ds_read_b128 v[44:47], v92
	s_waitcnt lgkmcnt(1)
	v_mul_f32_e32 v49, v26, v49
	v_fmac_f32_e32 v49, v16, v48
	v_fmac_f32_e32 v49, v17, v50
	v_fmac_f32_e32 v49, v19, v51
	v_add_f32_e32 v43, v43, v49
	ds_read_b128 v[48:51], v93
	s_waitcnt lgkmcnt(1)
	v_mul_f32_e32 v45, v18, v45
	v_fmac_f32_e32 v45, v12, v44
	v_fmac_f32_e32 v45, v13, v46
	v_fmac_f32_e32 v45, v15, v47
	v_add_f32_e32 v43, v43, v45
	ds_read_b128 v[44:47], v94
	s_waitcnt lgkmcnt(1)
	v_mul_f32_e32 v49, v14, v49
	v_fmac_f32_e32 v49, v8, v48
	v_fmac_f32_e32 v49, v9, v50
	v_fmac_f32_e32 v49, v11, v51
	s_waitcnt lgkmcnt(0)
	v_mul_f32_e32 v45, v10, v45
	v_fmac_f32_e32 v45, v4, v44
	v_fmac_f32_e32 v45, v5, v46
	v_add_f32_e32 v43, v43, v49
	v_fmac_f32_e32 v45, v7, v47
	v_add_f32_e32 v43, v43, v45
	ds_read_b128 v[44:47], v97
	ds_read_b128 v[48:51], v98
	ds_read_b128 v[52:55], v95
	ds_read_b128 v[56:59], v96
	ds_read_b128 v[60:63], v99
	ds_read_b128 v[76:79], v100
	ds_read_b128 v[152:155], v101
	ds_read_b128 v[156:159], v102
	s_waitcnt lgkmcnt(4)
	v_mul_f32_e32 v57, v64, v57
	v_fmac_f32_e32 v57, v20, v56
	v_fmac_f32_e32 v57, v21, v58
	v_fmac_f32_e32 v57, v23, v59
	v_add_f32_e32 v56, 0, v57
	s_waitcnt lgkmcnt(0)
	v_mul_f32_e32 v57, v29, v157
	v_fmac_f32_e32 v57, v22, v156
	v_fmac_f32_e32 v57, v28, v158
	v_fmac_f32_e32 v57, v31, v159
	v_add_f32_e32 v56, v57, v56
	v_mul_f32_e32 v57, v33, v153
	v_fmac_f32_e32 v57, v30, v152
	v_fmac_f32_e32 v57, v32, v154
	v_fmac_f32_e32 v57, v35, v155
	v_add_f32_e32 v56, v57, v56
	v_mul_f32_e32 v57, v34, v77
	v_fmac_f32_e32 v57, v24, v76
	v_fmac_f32_e32 v57, v25, v78
	v_fmac_f32_e32 v57, v27, v79
	v_add_f32_e32 v56, v57, v56
	v_mul_f32_e32 v57, v26, v61
	v_fmac_f32_e32 v57, v16, v60
	v_mul_f32_e32 v49, v18, v49
	v_fmac_f32_e32 v57, v17, v62
	v_fmac_f32_e32 v49, v12, v48
	v_mul_f32_e32 v45, v14, v45
	v_fmac_f32_e32 v57, v19, v63
	v_fmac_f32_e32 v49, v13, v50
	v_fmac_f32_e32 v45, v8, v44
	v_add_f32_e32 v56, v57, v56
	v_fmac_f32_e32 v49, v15, v51
	v_fmac_f32_e32 v45, v9, v46
	v_add_f32_e32 v48, v49, v56
	v_fmac_f32_e32 v45, v11, v47
	v_add_f32_e32 v44, v45, v48
	v_mul_f32_e32 v45, v10, v53
	v_fmac_f32_e32 v45, v4, v52
	v_fmac_f32_e32 v45, v5, v54
	v_fmac_f32_e32 v45, v7, v55
	v_add_f32_e32 v65, v45, v44
	ds_read_b128 v[44:47], v105
	ds_read_b128 v[48:51], v106
	ds_read_b128 v[52:55], v103
	ds_read_b128 v[56:59], v104
	ds_read_b128 v[60:63], v107
	ds_read_b128 v[76:79], v108
	ds_read_b128 v[152:155], v109
	ds_read_b128 v[156:159], v110
	s_waitcnt lgkmcnt(4)
	v_mul_f32_e32 v57, v64, v57
	v_fmac_f32_e32 v57, v20, v56
	v_fmac_f32_e32 v57, v21, v58
	v_fmac_f32_e32 v57, v23, v59
	v_add_f32_e32 v56, 0, v57
	s_waitcnt lgkmcnt(0)
	v_mul_f32_e32 v57, v29, v157
	v_fmac_f32_e32 v57, v22, v156
	v_fmac_f32_e32 v57, v28, v158
	v_fmac_f32_e32 v57, v31, v159
	v_add_f32_e32 v56, v57, v56
	v_mul_f32_e32 v57, v33, v153
	v_fmac_f32_e32 v57, v30, v152
	v_fmac_f32_e32 v57, v32, v154
	v_fmac_f32_e32 v57, v35, v155
	v_add_f32_e32 v56, v57, v56
	v_mul_f32_e32 v57, v34, v77
	v_fmac_f32_e32 v57, v24, v76
	v_fmac_f32_e32 v57, v25, v78
	v_fmac_f32_e32 v57, v27, v79
	v_add_f32_e32 v56, v57, v56
	v_mul_f32_e32 v57, v26, v61
	v_fmac_f32_e32 v57, v16, v60
	v_mul_f32_e32 v49, v18, v49
	v_fmac_f32_e32 v57, v17, v62
	v_fmac_f32_e32 v49, v12, v48
	v_mul_f32_e32 v45, v14, v45
	v_fmac_f32_e32 v57, v19, v63
	v_fmac_f32_e32 v49, v13, v50
	v_fmac_f32_e32 v45, v8, v44
	v_add_f32_e32 v56, v57, v56
	v_fmac_f32_e32 v49, v15, v51
	v_fmac_f32_e32 v45, v9, v46
	v_add_f32_e32 v48, v49, v56
	v_fmac_f32_e32 v45, v11, v47
	v_add_f32_e32 v44, v45, v48
	v_mul_f32_e32 v45, v10, v53
	v_fmac_f32_e32 v45, v4, v52
	v_fmac_f32_e32 v45, v5, v54
	v_fmac_f32_e32 v45, v7, v55
	v_add_f32_e32 v66, v45, v44
	ds_read_b128 v[44:47], v113
	ds_read_b128 v[48:51], v114
	ds_read_b128 v[52:55], v111
	ds_read_b128 v[56:59], v112
	ds_read_b128 v[60:63], v115
	ds_read_b128 v[76:79], v116
	ds_read_b128 v[152:155], v117
	ds_read_b128 v[156:159], v118
	s_waitcnt lgkmcnt(4)
; template <int MODE>
; DEVI void phase_rows(const Params& p, int l, char* smem) {
;     ...
;             for (int e = 0; e < 16; ++e) { float t = 0.f;
; #pragma unroll
;                 for (int i = 0; i < 8; ++i) { const f32x4 w = *(const f32x4*)(wT + e * 2048 + i * 256 + lane * 4);
;                     t += v[i * 4] * w[0] + v[i * 4 + 1] * w[1] + v[i * 4 + 2] * w[2] + v[i * 4 + 3] * w[3]; }
;                 a[e] = t; if ((e & 3) == 3) __builtin_amdgcn_sched_barrier(0); }
	v_mul_f32_e32 v57, v64, v57
	v_fmac_f32_e32 v57, v20, v56
	v_fmac_f32_e32 v57, v21, v58
	v_fmac_f32_e32 v57, v23, v59
	v_add_f32_e32 v56, 0, v57
	s_waitcnt lgkmcnt(0)
	v_mul_f32_e32 v57, v29, v157
	v_fmac_f32_e32 v57, v22, v156
	v_fmac_f32_e32 v57, v28, v158
	v_fmac_f32_e32 v57, v31, v159
	v_add_f32_e32 v56, v57, v56
	v_mul_f32_e32 v57, v33, v153
	v_fmac_f32_e32 v57, v30, v152
	v_fmac_f32_e32 v57, v32, v154
	v_fmac_f32_e32 v57, v35, v155
	v_add_f32_e32 v56, v57, v56
	v_mul_f32_e32 v57, v34, v77
	v_fmac_f32_e32 v57, v24, v76
	v_fmac_f32_e32 v57, v25, v78
	v_fmac_f32_e32 v57, v27, v79
	v_add_f32_e32 v56, v57, v56
	v_mul_f32_e32 v57, v26, v61
	v_fmac_f32_e32 v57, v16, v60
	v_mul_f32_e32 v49, v18, v49
	v_fmac_f32_e32 v57, v17, v62
	v_fmac_f32_e32 v49, v12, v48
	v_mul_f32_e32 v45, v14, v45
	v_fmac_f32_e32 v57, v19, v63
	v_fmac_f32_e32 v49, v13, v50
	v_fmac_f32_e32 v45, v8, v44
	v_add_f32_e32 v56, v57, v56
	v_fmac_f32_e32 v49, v15, v51
	v_fmac_f32_e32 v45, v9, v46
	v_add_f32_e32 v48, v49, v56
	v_fmac_f32_e32 v45, v11, v47
	v_add_f32_e32 v44, v45, v48
	v_mul_f32_e32 v45, v10, v53
	v_fmac_f32_e32 v45, v4, v52
	v_fmac_f32_e32 v45, v5, v54
	v_fmac_f32_e32 v45, v7, v55
	v_add_f32_e32 v67, v45, v44
	ds_read_b128 v[44:47], v119
	ds_read_b128 v[48:51], v120
	ds_read_b128 v[52:55], v121
	s_waitcnt lgkmcnt(2)
	v_mul_f32_e32 v45, v64, v45
	s_waitcnt lgkmcnt(1)
	v_mul_f32_e32 v49, v29, v49
	v_fmac_f32_e32 v45, v20, v44
	v_fmac_f32_e32 v49, v22, v48
	v_fmac_f32_e32 v45, v21, v46
	v_fmac_f32_e32 v45, v23, v47
	v_fmac_f32_e32 v49, v28, v50
	v_add_f32_e32 v44, 0, v45
	v_fmac_f32_e32 v49, v31, v51
	v_add_f32_e32 v48, v44, v49
	ds_read_b128 v[44:47], v122
	s_waitcnt lgkmcnt(1)
	v_mul_f32_e32 v49, v33, v53
	v_fmac_f32_e32 v49, v30, v52
	v_fmac_f32_e32 v49, v32, v54
	v_fmac_f32_e32 v49, v35, v55
	v_add_f32_e32 v52, v48, v49
	ds_read_b128 v[48:51], v123
	s_waitcnt lgkmcnt(1)
	v_mul_f32_e32 v45, v34, v45
	v_fmac_f32_e32 v45, v24, v44
	v_fmac_f32_e32 v45, v25, v46
	v_fmac_f32_e32 v45, v27, v47
	v_add_f32_e32 v52, v52, v45
	ds_read_b128 v[44:47], v124
	s_waitcnt lgkmcnt(1)
	v_mul_f32_e32 v49, v26, v49
	v_fmac_f32_e32 v49, v16, v48
	v_fmac_f32_e32 v49, v17, v50
	v_fmac_f32_e32 v49, v19, v51
	v_add_f32_e32 v52, v52, v49
	ds_read_b128 v[48:51], v125
	s_waitcnt lgkmcnt(1)
	v_mul_f32_e32 v45, v18, v45
	v_fmac_f32_e32 v45, v12, v44
	v_fmac_f32_e32 v45, v13, v46
	v_fmac_f32_e32 v45, v15, v47
	v_add_f32_e32 v52, v52, v45
	ds_read_b128 v[44:47], v126
	s_waitcnt lgkmcnt(1)
	v_mul_f32_e32 v49, v14, v49
	v_fmac_f32_e32 v49, v8, v48
	v_fmac_f32_e32 v49, v9, v50
	v_fmac_f32_e32 v49, v11, v51
	s_waitcnt lgkmcnt(0)
	v_mul_f32_e32 v45, v10, v45
	v_fmac_f32_e32 v45, v4, v44
	v_fmac_f32_e32 v45, v5, v46
	v_add_f32_e32 v48, v52, v49
	v_fmac_f32_e32 v45, v7, v47
	v_add_f32_e32 v69, v48, v45
	ds_read_b128 v[44:47], v129
	ds_read_b128 v[48:51], v130
	ds_read_b128 v[52:55], v127
	ds_read_b128 v[56:59], v128
	ds_read_b128 v[60:63], v131
	ds_read_b128 v[76:79], v132
	ds_read_b128 v[152:155], v133
	ds_read_b128 v[156:159], v134
	s_waitcnt lgkmcnt(4)
	v_mul_f32_e32 v57, v64, v57
	v_fmac_f32_e32 v57, v20, v56
	v_fmac_f32_e32 v57, v21, v58
	v_fmac_f32_e32 v57, v23, v59
	v_add_f32_e32 v56, 0, v57
	s_waitcnt lgkmcnt(0)
	v_mul_f32_e32 v57, v29, v157
	v_fmac_f32_e32 v57, v22, v156
	v_fmac_f32_e32 v57, v28, v158
	v_fmac_f32_e32 v57, v31, v159
	v_add_f32_e32 v56, v57, v56
	v_mul_f32_e32 v57, v33, v153
	v_fmac_f32_e32 v57, v30, v152
	v_fmac_f32_e32 v57, v32, v154
	v_fmac_f32_e32 v57, v35, v155
	v_add_f32_e32 v56, v57, v56
	v_mul_f32_e32 v57, v34, v77
	v_fmac_f32_e32 v57, v24, v76
	v_fmac_f32_e32 v57, v25, v78
	v_fmac_f32_e32 v57, v27, v79
	v_add_f32_e32 v56, v57, v56
	v_mul_f32_e32 v57, v26, v61
	v_fmac_f32_e32 v57, v16, v60
	v_mul_f32_e32 v49, v18, v49
	v_fmac_f32_e32 v57, v17, v62
	v_fmac_f32_e32 v49, v12, v48
	v_mul_f32_e32 v45, v14, v45
	v_fmac_f32_e32 v57, v19, v63
	v_fmac_f32_e32 v49, v13, v50
	v_fmac_f32_e32 v45, v8, v44
	v_add_f32_e32 v56, v57, v56
	v_fmac_f32_e32 v49, v15, v51
	v_fmac_f32_e32 v45, v9, v46
	v_add_f32_e32 v48, v49, v56
	v_fmac_f32_e32 v45, v11, v47
	v_add_f32_e32 v44, v45, v48
	v_mul_f32_e32 v45, v10, v53
	v_fmac_f32_e32 v45, v4, v52
	v_fmac_f32_e32 v45, v5, v54
	v_fmac_f32_e32 v45, v7, v55
	v_add_f32_e32 v80, v45, v44
	ds_read_b128 v[44:47], v137
	ds_read_b128 v[48:51], v138
	ds_read_b128 v[52:55], v135
	ds_read_b128 v[56:59], v136
	ds_read_b128 v[60:63], v139
	ds_read_b128 v[76:79], v140
	ds_read_b128 v[152:155], v141
	ds_read_b128 v[156:159], v142
	s_waitcnt lgkmcnt(4)
	v_mul_f32_e32 v57, v64, v57
	v_fmac_f32_e32 v57, v20, v56
	v_fmac_f32_e32 v57, v21, v58
	v_fmac_f32_e32 v57, v23, v59
	v_add_f32_e32 v56, 0, v57
	s_waitcnt lgkmcnt(0)
	v_mul_f32_e32 v57, v29, v157
	v_fmac_f32_e32 v57, v22, v156
	v_fmac_f32_e32 v57, v28, v158
	v_fmac_f32_e32 v57, v31, v159
	v_add_f32_e32 v56, v57, v56
	v_mul_f32_e32 v57, v33, v153
	v_fmac_f32_e32 v57, v30, v152
	v_fmac_f32_e32 v57, v32, v154
	v_fmac_f32_e32 v57, v35, v155
	v_add_f32_e32 v56, v57, v56
	v_mul_f32_e32 v57, v34, v77
	v_fmac_f32_e32 v57, v24, v76
	v_fmac_f32_e32 v57, v25, v78
	v_fmac_f32_e32 v57, v27, v79
	v_add_f32_e32 v56, v57, v56
	v_mul_f32_e32 v57, v26, v61
	v_fmac_f32_e32 v57, v16, v60
	v_mul_f32_e32 v49, v18, v49
	v_fmac_f32_e32 v57, v17, v62
	v_fmac_f32_e32 v49, v12, v48
	v_mul_f32_e32 v45, v14, v45
	v_fmac_f32_e32 v57, v19, v63
	v_fmac_f32_e32 v49, v13, v50
	v_fmac_f32_e32 v45, v8, v44
	v_add_f32_e32 v56, v57, v56
	v_fmac_f32_e32 v49, v15, v51
	v_fmac_f32_e32 v45, v9, v46
	v_add_f32_e32 v48, v49, v56
	v_fmac_f32_e32 v45, v11, v47
	v_add_f32_e32 v44, v45, v48
	v_mul_f32_e32 v45, v10, v53
	v_fmac_f32_e32 v45, v4, v52
	v_fmac_f32_e32 v45, v5, v54
	v_fmac_f32_e32 v45, v7, v55
	v_add_f32_e32 v81, v45, v44
	ds_read_b128 v[44:47], v145
	ds_read_b128 v[48:51], v146
	ds_read_b128 v[52:55], v143
	ds_read_b128 v[56:59], v144
	ds_read_b128 v[60:63], v147
	ds_read_b128 v[76:79], v148
	ds_read_b128 v[152:155], v149
	ds_read_b128 v[156:159], v150
	s_waitcnt lgkmcnt(4)
; template <int MODE>
; DEVI void phase_rows(const Params& p, int l, char* smem) {
;     ...
;             const bool b5 = (lane & 32) != 0, b4 = (lane & 16) != 0, b3 = (lane & 8) != 0, b2 = (lane & 4) != 0;
;             float s8[8], s4[4], s2[2], s1;
; #pragma unroll
;             for (int i = 0; i < 8; ++i) { const float keep = b5 ? a[8 + i] : a[i], give = b5 ? a[i] : a[8 + i]; s8[i] = keep + __shfl_xor(give, 32); }
; #pragma unroll
;             for (int i = 0; i < 4; ++i) { const float keep = b4 ? s8[4 + i] : s8[i], give = b4 ? s8[i] : s8[4 + i]; s4[i] = keep + __shfl_xor(give, 16); }
; #pragma unroll
;             for (int i = 0; i < 2; ++i) { const float keep = b3 ? s4[2 + i] : s4[i], give = b3 ? s4[i] : s4[2 + i]; s2[i] = keep + __shfl_xor(give, 8); }
;             { const float keep = b2 ? s2[1] : s2[0], give = b2 ? s2[0] : s2[1]; s1 = keep + __shfl_xor(give, 4); }
;             s1 += __shfl_xor(s1, 2); s1 += __shfl_xor(s1, 1);
;             float mx = s1;
; #pragma unroll
;             for (int off = 32; off >= 4; off >>= 1) mx = fmaxf(mx, __shfl_xor(mx, off));
;             const float ex = expf(s1 - mx); float den = ex;
; #pragma unroll
;             for (int off = 32; off >= 4; off >>= 1) den += __shfl_xor(den, off);
;             const int eidx = (b5 ? 8 : 0) + (b4 ? 4 : 0) + (b3 ? 2 : 0) + (b2 ? 1 : 0);
;             if ((lane & 3) == 0) ((float*)(p.ws + WS_AFF))[((size_t)b * 16 + eidx) * KEYS + tok] = ex / den;
	v_mul_f32_e32 v57, v64, v57
	v_fmac_f32_e32 v57, v20, v56
	v_fmac_f32_e32 v57, v21, v58
	v_fmac_f32_e32 v57, v23, v59
	s_waitcnt lgkmcnt(0)
	v_mul_f32_e32 v21, v29, v157
	v_fmac_f32_e32 v21, v22, v156
	v_fmac_f32_e32 v21, v28, v158
	v_add_f32_e32 v20, 0, v57
	v_fmac_f32_e32 v21, v31, v159
	v_add_f32_e32 v20, v21, v20
	v_mul_f32_e32 v21, v33, v153
	v_fmac_f32_e32 v21, v30, v152
	v_fmac_f32_e32 v21, v32, v154
	v_fmac_f32_e32 v21, v35, v155
	v_add_f32_e32 v20, v21, v20
	v_mul_f32_e32 v21, v34, v77
	v_fmac_f32_e32 v21, v24, v76
	v_fmac_f32_e32 v21, v25, v78
	v_fmac_f32_e32 v21, v27, v79
	v_add_f32_e32 v20, v21, v20
	v_mul_f32_e32 v21, v26, v61
	v_fmac_f32_e32 v21, v16, v60
	v_fmac_f32_e32 v21, v17, v62
	v_mul_f32_e32 v17, v18, v49
	v_fmac_f32_e32 v17, v12, v48
	v_fmac_f32_e32 v17, v13, v50
	v_mul_f32_e32 v13, v14, v45
	v_fmac_f32_e32 v13, v8, v44
	v_fmac_f32_e32 v21, v19, v63
	v_fmac_f32_e32 v13, v9, v46
	v_mul_f32_e32 v9, v10, v53
	v_add_f32_e32 v16, v21, v20
	v_fmac_f32_e32 v17, v15, v51
	v_fmac_f32_e32 v9, v4, v52
	v_add_f32_e32 v12, v17, v16
	v_fmac_f32_e32 v13, v11, v47
	v_fmac_f32_e32 v9, v5, v54
	v_add_f32_e32 v8, v13, v12
	v_fmac_f32_e32 v9, v7, v55
	v_add_f32_e32 v4, v9, v8
	v_cndmask_b32_e64 v5, v43, v6, s[38:39]
	v_cndmask_b32_e64 v6, v6, v43, s[38:39]
	ds_bpermute_b32 v6, v1, v6
	v_cndmask_b32_e64 v7, v36, v65, s[38:39]
	ds_bpermute_b32 v7, v1, v7
	v_cndmask_b32_e64 v8, v37, v66, s[38:39]
	ds_bpermute_b32 v8, v1, v8
	v_cndmask_b32_e64 v9, v38, v67, s[38:39]
	ds_bpermute_b32 v9, v1, v9
	v_cndmask_b32_e64 v10, v39, v69, s[38:39]
	ds_bpermute_b32 v10, v1, v10
	v_cndmask_b32_e64 v11, v40, v80, s[38:39]
	s_waitcnt lgkmcnt(4)
	v_add_f32_e32 v5, v5, v6
	v_cndmask_b32_e64 v6, v65, v36, s[38:39]
	ds_bpermute_b32 v11, v1, v11
	v_cndmask_b32_e64 v12, v41, v81, s[38:39]
	s_waitcnt lgkmcnt(4)
	v_add_f32_e32 v6, v6, v7
	v_cndmask_b32_e64 v7, v66, v37, s[38:39]
	ds_bpermute_b32 v12, v1, v12
	s_waitcnt lgkmcnt(4)
	v_add_f32_e32 v7, v7, v8
	v_cndmask_b32_e64 v8, v67, v38, s[38:39]
	s_waitcnt lgkmcnt(3)
	v_add_f32_e32 v8, v8, v9
	v_cndmask_b32_e64 v9, v69, v39, s[38:39]
	s_waitcnt lgkmcnt(2)
	v_add_f32_e32 v9, v9, v10
	v_cndmask_b32_e64 v10, v80, v40, s[38:39]
	s_waitcnt lgkmcnt(1)
	v_add_f32_e32 v10, v10, v11
	v_cndmask_b32_e64 v11, v81, v41, s[38:39]
	s_waitcnt lgkmcnt(0)
	v_add_f32_e32 v11, v11, v12
	v_cndmask_b32_e64 v12, v4, v42, s[38:39]
	v_cndmask_b32_e64 v4, v42, v4, s[38:39]
	ds_bpermute_b32 v4, v1, v4
	s_mov_b32 s4, 0xc2ce8ed0
	s_waitcnt lgkmcnt(0)
	v_add_f32_e32 v4, v12, v4
	v_cndmask_b32_e64 v12, v9, v5, s[40:41]
	v_cndmask_b32_e64 v5, v5, v9, s[40:41]
	v_cndmask_b32_e64 v9, v10, v6, s[40:41]
	v_cndmask_b32_e64 v6, v6, v10, s[40:41]
	ds_bpermute_b32 v6, v75, v6
	ds_bpermute_b32 v5, v75, v5
	s_waitcnt lgkmcnt(1)
	v_add_f32_e32 v6, v9, v6
	v_cndmask_b32_e64 v9, v11, v7, s[40:41]
	v_cndmask_b32_e64 v7, v7, v11, s[40:41]
	ds_bpermute_b32 v7, v75, v7
	s_waitcnt lgkmcnt(1)
	v_add_f32_e32 v5, v12, v5
	s_waitcnt lgkmcnt(0)
	v_add_f32_e32 v7, v9, v7
	v_cndmask_b32_e64 v9, v4, v8, s[40:41]
	v_cndmask_b32_e64 v4, v8, v4, s[40:41]
	ds_bpermute_b32 v4, v75, v4
	v_cndmask_b32_e64 v8, v7, v5, s[42:43]
	v_cndmask_b32_e64 v5, v5, v7, s[42:43]
	ds_bpermute_b32 v5, v82, v5
	s_waitcnt lgkmcnt(1)
	v_add_f32_e32 v4, v9, v4
	v_cndmask_b32_e64 v7, v4, v6, s[42:43]
	v_cndmask_b32_e64 v4, v6, v4, s[42:43]
	ds_bpermute_b32 v4, v82, v4
	s_waitcnt lgkmcnt(1)
	v_add_f32_e32 v5, v8, v5
	s_waitcnt lgkmcnt(0)
	v_add_f32_e32 v4, v7, v4
	v_cndmask_b32_e64 v6, v4, v5, s[44:45]
	v_cndmask_b32_e64 v4, v5, v4, s[44:45]
	ds_bpermute_b32 v4, v83, v4
	s_waitcnt lgkmcnt(0)
	v_add_f32_e32 v4, v6, v4
	ds_bpermute_b32 v5, v84, v4
	s_waitcnt lgkmcnt(0)
	v_add_f32_e32 v4, v4, v5
	ds_bpermute_b32 v5, v85, v4
	s_waitcnt lgkmcnt(0)
	v_add_f32_e32 v4, v4, v5
	ds_bpermute_b32 v5, v1, v4
	s_waitcnt lgkmcnt(0)
	v_max_f32_e32 v5, v5, v5
	v_max_f32_e32 v5, v4, v5
	ds_bpermute_b32 v6, v75, v5
	s_waitcnt lgkmcnt(0)
	v_max_f32_e32 v6, v6, v6
	v_max_f32_e32 v5, v5, v6
	ds_bpermute_b32 v6, v82, v5
	s_waitcnt lgkmcnt(0)
	v_max_f32_e32 v6, v6, v6
	v_max_f32_e32 v5, v5, v6
	ds_bpermute_b32 v6, v83, v5
	s_waitcnt lgkmcnt(0)
	v_max_f32_e32 v6, v6, v6
	v_max_f32_e32 v5, v5, v6
	v_sub_f32_e32 v4, v4, v5
	v_mul_f32_e32 v5, 0x3fb8aa3b, v4
	v_fma_f32 v6, v4, s72, -v5
	v_rndne_f32_e32 v7, v5
	v_fmac_f32_e32 v6, 0x32a5705f, v4
	v_sub_f32_e32 v5, v5, v7
	v_add_f32_e32 v5, v5, v6
	v_exp_f32_e32 v5, v5
	v_cvt_i32_f32_e32 v6, v7
	v_cmp_ngt_f32_e64 s[50:51], s4, v4
	s_mov_b32 s4, 0x42b17218
	v_ldexp_f32 v5, v5, v6
	v_cndmask_b32_e64 v5, 0, v5, s[50:51]
	v_cmp_nlt_f32_e64 s[50:51], s4, v4
	v_mov_b32_e32 v4, 0x7f800000
	s_nop 0
	v_cndmask_b32_e64 v4, v4, v5, s[50:51]
	ds_bpermute_b32 v5, v1, v4
	s_waitcnt lgkmcnt(0)
	v_add_f32_e32 v5, v4, v5
	ds_bpermute_b32 v6, v75, v5
	s_waitcnt lgkmcnt(0)
	v_add_f32_e32 v5, v5, v6
	ds_bpermute_b32 v6, v82, v5
	s_waitcnt lgkmcnt(0)
	v_add_f32_e32 v5, v5, v6
	ds_bpermute_b32 v6, v83, v5
	s_and_saveexec_b64 s[16:17], s[46:47]
	s_cbranch_execz .LBB0_1042
	s_movk_i32 s4, 0x800
	s_waitcnt lgkmcnt(0)
	v_add_f32_e32 v5, v5, v6
	v_and_b32_e32 v7, 0x7ff, v68
	v_or_b32_sdwa v8, v68, s4 dst_sel:DWORD dst_unused:UNUSED_PAD src0_sel:BYTE_0 src1_sel:DWORD
	v_div_scale_f32 v6, s[4:5], v5, v5, v4
	v_cndmask_b32_e32 v7, v8, v7, vcc
	v_rcp_f32_e32 v8, v6
	v_add_u32_e32 v9, 0xffffe000, v68
	v_lshrrev_b32_e32 v9, 8, v9
	v_cndmask_b32_e32 v9, v9, v151, vcc
	v_fma_f32 v10, -v6, v8, 1.0
	v_fmac_f32_e32 v8, v10, v8
	v_div_scale_f32 v10, vcc, v4, v5, v4
	v_mul_f32_e32 v11, v10, v8
	v_fma_f32 v12, -v6, v11, v10
	v_fmac_f32_e32 v11, v12, v8
	v_fma_f32 v6, -v6, v11, v10
	v_div_fmas_f32 v6, v6, v8, v11
	v_div_fixup_f32 v8, v6, v5, v4
	v_lshl_or_b32 v6, v9, 4, v74
	v_mov_b64_e32 v[4:5], s[6:7]
	s_movk_i32 s4, 0x2400
	v_mad_i64_i32 v[4:5], s[4:5], v6, s4, v[4:5]
	v_lshlrev_b32_e32 v6, 2, v7
	v_mov_b32_e32 v7, v3
	v_lshl_add_u64 v[4:5], v[4:5], 0, v[6:7]
	global_store_dword v[4:5], v8, off
	s_branch .LBB0_1042

; DEVI float bflo(unsigned w) { return __uint_as_float(w << 16); }
; DEVI float bfhi(unsigned w) { return __uint_as_float(w & 0xffff0000u); }
; template <int MODE>
; DEVI void phase_rows(const Params& p, int l, char* smem) {
;     ...
;             {   u32x2 w0[8], w1[8], w2[8], w3[8];
; #pragma unroll
;                 for (int i = 0; i < 8; ++i) { w0[i] = *(const u32x2*)(y0 + i * 256 + lane * 4); w1[i] = *(const u32x2*)(y1 + i * 256 + lane * 4);
;                     w2[i] = *(const u32x2*)(y2 + i * 256 + lane * 4); w3[i] = *(const u32x2*)(y3 + i * 256 + lane * 4); }
;                 const float f0 = ny > 0 ? 1.f : 0.f, f1 = ny > 1 ? 1.f : 0.f, f2 = ny > 2 ? 1.f : 0.f, f3 = ny > 3 ? 1.f : 0.f;
; #pragma unroll
;                 for (int i = 0; i < 8; ++i) {
;                     cacc[i * 4] += f0 * bflo(w0[i][0]) + f1 * bflo(w1[i][0]) + f2 * bflo(w2[i][0]) + f3 * bflo(w3[i][0]);
;                     cacc[i * 4 + 1] += f0 * bfhi(w0[i][0]) + f1 * bfhi(w1[i][0]) + f2 * bfhi(w2[i][0]) + f3 * bfhi(w3[i][0]);
;                     cacc[i * 4 + 2] += f0 * bflo(w0[i][1]) + f1 * bflo(w1[i][1]) + f2 * bflo(w2[i][1]) + f3 * bflo(w3[i][1]);
;                     cacc[i * 4 + 3] += f0 * bfhi(w0[i][1]) + f1 * bfhi(w1[i][1]) + f2 * bfhi(w2[i][1]) + f3 * bfhi(w3[i][1]); }
;             }
;             const float* gf = mrow + 10240;
; #pragma unroll
;             for (int i = 0; i < 8; ++i) { const f32x4 g = *(const f32x4*)(gf + i * 256 + lane * 4);
;                 v[i * 4] += g[0] * cacc[i * 4]; v[i * 4 + 1] += g[1] * cacc[i * 4 + 1]; v[i * 4 + 2] += g[2] * cacc[i * 4 + 2]; v[i * 4 + 3] += g[3] * cacc[i * 4 + 3]; }
.LBB0_1467:
	s_or_b64 exec, exec, s[16:17]
	v_lshlrev_b32_e32 v2, 1, v50
	v_lshl_add_u64 v[96:97], v[78:79], 0, v[2:3]
	v_lshl_add_u64 v[98:99], v[74:75], 0, v[2:3]
	global_load_dwordx2 v[106:107], v[96:97], off
	global_load_dwordx2 v[108:109], v[98:99], off
	global_load_dwordx2 v[120:121], v[96:97], off offset:512
	global_load_dwordx2 v[122:123], v[98:99], off offset:512
	v_lshlrev_b32_e32 v104, 16, v46
	v_and_b32_e32 v105, 0xffff0000, v46
	v_lshlrev_b32_e32 v102, 16, v47
	v_and_b32_e32 v103, 0xffff0000, v47
	global_load_dwordx2 v[46:47], v[96:97], off offset:1024
	global_load_dwordx2 v[126:127], v[98:99], off offset:1024
	v_mul_hi_i32_i24_e32 v113, 0xc000, v49
	v_mul_i32_i24_e32 v112, 0xc000, v49
	v_lshlrev_b32_e32 v100, 16, v70
	v_and_b32_e32 v101, 0xffff0000, v70
	v_lshlrev_b32_e32 v110, 16, v71
	v_and_b32_e32 v111, 0xffff0000, v71
	v_lshlrev_b32_e32 v124, 16, v68
	v_and_b32_e32 v125, 0xffff0000, v68
	v_lshlrev_b32_e32 v118, 16, v69
	v_and_b32_e32 v119, 0xffff0000, v69
	v_lshlrev_b32_e32 v94, 16, v44
	v_and_b32_e32 v95, 0xffff0000, v44
	v_lshlrev_b32_e32 v92, 16, v45
	v_and_b32_e32 v93, 0xffff0000, v45
	v_lshlrev_b32_e32 v90, 16, v42
	v_and_b32_e32 v91, 0xffff0000, v42
	global_load_dwordx2 v[44:45], v[96:97], off offset:1536
	global_load_dwordx2 v[128:129], v[98:99], off offset:1536
	v_lshlrev_b32_e32 v88, 16, v43
	v_and_b32_e32 v89, 0xffff0000, v43
	v_lshlrev_b32_e32 v86, 16, v40
	v_and_b32_e32 v87, 0xffff0000, v40
	v_lshlrev_b32_e32 v84, 16, v41
	v_and_b32_e32 v85, 0xffff0000, v41
	v_lshlrev_b32_e32 v82, 16, v38
	v_and_b32_e32 v83, 0xffff0000, v38
	global_load_dwordx2 v[40:41], v[96:97], off offset:2048
	global_load_dwordx2 v[42:43], v[98:99], off offset:2048
	v_lshlrev_b32_e32 v80, 16, v39
	v_and_b32_e32 v81, 0xffff0000, v39
	v_lshlrev_b32_e32 v70, 16, v36
	v_and_b32_e32 v71, 0xffff0000, v36
	v_lshlrev_b32_e32 v68, 16, v37
	v_and_b32_e32 v69, 0xffff0000, v37
	global_load_dwordx2 v[36:37], v[96:97], off offset:2560
	global_load_dwordx2 v[38:39], v[98:99], off offset:2560
	v_cmp_lt_u32_e32 vcc, 2, v116
	v_lshl_add_u64 v[72:73], v[72:73], 0, v[2:3]
	v_lshl_add_u64 v[76:77], v[76:77], 0, v[2:3]
	v_lshl_add_u64 v[134:135], s[82:83], 0, v[112:113]
	v_lshlrev_b32_e32 v2, 2, v50
	v_cndmask_b32_e64 v74, 0, 1.0, vcc
	v_cmp_lt_u32_e32 vcc, 3, v116
	v_lshl_add_u64 v[134:135], v[134:135], 0, v[2:3]
	global_load_dwordx2 v[138:139], v[96:97], off offset:3072
	global_load_dwordx2 v[144:145], v[98:99], off offset:3072
	v_cndmask_b32_e64 v78, 0, 1.0, vcc
	v_add_co_u32_e32 v202, vcc, s62, v134
	global_load_dwordx2 v[180:181], v[96:97], off offset:3584
	global_load_dwordx2 v[182:183], v[98:99], off offset:3584
	global_load_dwordx2 v[184:185], v[72:73], off
	global_load_dwordx2 v[188:189], v[72:73], off offset:512
	global_load_dwordx2 v[190:191], v[72:73], off offset:1024
	global_load_dwordx2 v[150:151], v[72:73], off offset:1536
	global_load_dwordx2 v[186:187], v[76:77], off
	global_load_dwordx2 v[192:193], v[76:77], off offset:512
	global_load_dwordx2 v[194:195], v[76:77], off offset:1024
	global_load_dwordx2 v[152:153], v[76:77], off offset:1536
	global_load_dwordx2 v[130:131], v[72:73], off offset:2048
	global_load_dwordx2 v[112:113], v[72:73], off offset:2560
	global_load_dwordx2 v[96:97], v[72:73], off offset:3072
	s_nop 0
	global_load_dwordx2 v[72:73], v[72:73], off offset:3584
	s_nop 0
	global_load_dwordx2 v[132:133], v[76:77], off offset:2048
	global_load_dwordx2 v[114:115], v[76:77], off offset:2560
	global_load_dwordx2 v[98:99], v[76:77], off offset:3072
	s_nop 0
	global_load_dwordx2 v[76:77], v[76:77], off offset:3584
	v_addc_co_u32_e32 v203, vcc, 0, v135, vcc
	global_load_dwordx4 v[168:171], v[202:203], off offset:-4096
	s_mov_b64 s[4:5], 0xe000
	v_cmp_eq_u32_e32 vcc, 0, v116
	v_add_u32_e32 v48, s44, v48
	s_waitcnt vmcnt(32)
	v_lshlrev_b32_e32 v198, 16, v106
	v_cndmask_b32_e64 v117, 1.0, 0, vcc
	v_cmp_lt_u32_e32 vcc, 1, v116
	s_waitcnt vmcnt(31)
	v_and_b32_e32 v199, 0xffff0000, v108
	v_lshlrev_b32_e32 v200, 16, v108
	v_cndmask_b32_e64 v116, 0, 1.0, vcc
	s_waitcnt vmcnt(28)
	v_lshlrev_b32_e32 v216, 16, v46
	v_and_b32_e32 v219, 0xffff0000, v46
	v_lshlrev_b32_e32 v220, 16, v47
	v_and_b32_e32 v229, 0xffff0000, v47
	v_lshl_add_u64 v[46:47], v[134:135], 0, s[4:5]
	global_load_dwordx4 v[172:175], v[46:47], off offset:1024
	global_load_dwordx4 v[176:179], v[46:47], off offset:2048
	v_and_b32_e32 v201, 0xffff0000, v106
	v_lshlrev_b32_e32 v204, 16, v107
	v_lshlrev_b32_e32 v206, 16, v109
	v_and_b32_e32 v207, 0xffff0000, v107
	v_and_b32_e32 v205, 0xffff0000, v109
	v_lshlrev_b32_e32 v208, 16, v120
	v_lshlrev_b32_e32 v210, 16, v122
	v_and_b32_e32 v211, 0xffff0000, v120
	v_and_b32_e32 v209, 0xffff0000, v122
	v_lshlrev_b32_e32 v212, 16, v121
	v_lshlrev_b32_e32 v214, 16, v123
	v_and_b32_e32 v215, 0xffff0000, v121
	v_and_b32_e32 v213, 0xffff0000, v123
	s_waitcnt vmcnt(28)
	v_lshlrev_b32_e32 v232, 16, v44
	v_and_b32_e32 v237, 0xffff0000, v44
	v_lshlrev_b32_e32 v240, 16, v45
	v_and_b32_e32 v243, 0xffff0000, v45
	v_lshlrev_b32_e32 v228, 16, v127
	v_and_b32_e32 v221, 0xffff0000, v127
	s_waitcnt vmcnt(26)
	v_lshlrev_b32_e32 v158, 16, v40
	s_waitcnt vmcnt(25)
	v_lshlrev_b32_e32 v160, 16, v42
	v_and_b32_e32 v161, 0xffff0000, v40
	v_and_b32_e32 v159, 0xffff0000, v42
	s_waitcnt vmcnt(20)
	v_lshlrev_b32_e32 v120, 16, v180
	s_waitcnt vmcnt(19)
; DEVI float bflo(unsigned w) { return __uint_as_float(w << 16); }
; DEVI float bfhi(unsigned w) { return __uint_as_float(w & 0xffff0000u); }
; template <int MODE>
; DEVI void phase_rows(const Params& p, int l, char* smem) {
;     ...
;                 const float f0 = ny > 0 ? 1.f : 0.f, f1 = ny > 1 ? 1.f : 0.f, f2 = ny > 2 ? 1.f : 0.f, f3 = ny > 3 ? 1.f : 0.f;
; #pragma unroll
;                 for (int i = 0; i < 8; ++i) {
;                     cacc[i * 4] += f0 * bflo(w0[i][0]) + f1 * bflo(w1[i][0]) + f2 * bflo(w2[i][0]) + f3 * bflo(w3[i][0]);
;                     cacc[i * 4 + 1] += f0 * bfhi(w0[i][0]) + f1 * bfhi(w1[i][0]) + f2 * bfhi(w2[i][0]) + f3 * bfhi(w3[i][0]);
;                     cacc[i * 4 + 2] += f0 * bflo(w0[i][1]) + f1 * bflo(w1[i][1]) + f2 * bflo(w2[i][1]) + f3 * bflo(w3[i][1]);
;                     cacc[i * 4 + 3] += f0 * bfhi(w0[i][1]) + f1 * bfhi(w1[i][1]) + f2 * bfhi(w2[i][1]) + f3 * bfhi(w3[i][1]); }
;             }
;             const float* gf = mrow + 10240;
; #pragma unroll
;             for (int i = 0; i < 8; ++i) { const f32x4 g = *(const f32x4*)(gf + i * 256 + lane * 4);
;                 v[i * 4] += g[0] * cacc[i * 4]; v[i * 4 + 1] += g[1] * cacc[i * 4 + 1]; v[i * 4 + 2] += g[2] * cacc[i * 4 + 2]; v[i * 4 + 3] += g[3] * cacc[i * 4 + 3]; }
	v_lshlrev_b32_e32 v122, 16, v182
	v_and_b32_e32 v123, 0xffff0000, v180
	v_lshlrev_b32_e32 v146, 16, v36
	v_and_b32_e32 v149, 0xffff0000, v36
	v_lshlrev_b32_e32 v140, 16, v37
	v_and_b32_e32 v143, 0xffff0000, v37
	v_and_b32_e32 v121, 0xffff0000, v182
	v_lshlrev_b32_e32 v106, 16, v181
	v_lshlrev_b32_e32 v108, 16, v183
	v_and_b32_e32 v109, 0xffff0000, v181
	v_and_b32_e32 v107, 0xffff0000, v183
	global_load_dwordx4 v[180:183], v[46:47], off offset:3072
	v_pk_mul_f32 v[36:37], v[116:117], v[198:199] op_sel:[1,0] op_sel_hi:[0,1]
	v_lshlrev_b32_e32 v148, 16, v38
	v_and_b32_e32 v147, 0xffff0000, v38
	v_lshlrev_b32_e32 v142, 16, v39
	v_and_b32_e32 v141, 0xffff0000, v39
	v_pk_fma_f32 v[36:37], v[116:117], v[200:201], v[36:37]
	s_waitcnt vmcnt(19)
	v_lshlrev_b32_e32 v38, 16, v184
	v_and_b32_e32 v39, 0xffff0000, v184
	v_pk_fma_f32 v[36:37], v[74:75], v[38:39], v[36:37] op_sel_hi:[0,1,1]
	s_waitcnt vmcnt(15)
	v_lshlrev_b32_e32 v38, 16, v186
	v_and_b32_e32 v39, 0xffff0000, v186
	v_pk_fma_f32 v[36:37], v[78:79], v[38:39], v[36:37] op_sel_hi:[0,1,1]
	v_pk_add_f32 v[4:5], v[4:5], v[36:37]
	v_lshlrev_b32_e32 v36, 16, v187
	s_waitcnt vmcnt(3)
	v_pk_fma_f32 v[100:101], v[4:5], v[168:169], v[100:101]
	v_lshlrev_b32_e32 v4, 16, v185
	v_and_b32_e32 v5, 0xffff0000, v185
	v_and_b32_e32 v37, 0xffff0000, v187
	global_load_dwordx4 v[184:187], v[202:203], off
	global_load_dwordx4 v[44:47], v[202:203], off offset:1024
	v_pk_mul_f32 v[38:39], v[116:117], v[204:205] op_sel:[1,0] op_sel_hi:[0,1]
	v_pk_fma_f32 v[38:39], v[116:117], v[206:207], v[38:39]
	v_lshlrev_b32_e32 v154, 16, v41
	v_pk_fma_f32 v[4:5], v[74:75], v[4:5], v[38:39] op_sel_hi:[0,1,1]
	v_lshlrev_b32_e32 v156, 16, v43
	v_and_b32_e32 v157, 0xffff0000, v41
	v_and_b32_e32 v155, 0xffff0000, v43
	v_pk_fma_f32 v[4:5], v[78:79], v[36:37], v[4:5] op_sel_hi:[0,1,1]
	global_load_dwordx4 v[40:43], v[202:203], off offset:2048
	global_load_dwordx4 v[36:39], v[202:203], off offset:3072
	v_lshlrev_b32_e32 v236, 16, v128
	v_and_b32_e32 v233, 0xffff0000, v128
	v_lshlrev_b32_e32 v136, 16, v144
	v_and_b32_e32 v135, 0xffff0000, v144
	v_lshlrev_b32_e32 v128, 16, v145
	v_and_b32_e32 v127, 0xffff0000, v145
	v_pk_mul_f32 v[144:145], v[116:117], v[208:209] op_sel:[1,0] op_sel_hi:[0,1]
	v_pk_fma_f32 v[144:145], v[116:117], v[210:211], v[144:145]
	v_lshlrev_b32_e32 v168, 16, v188
	v_and_b32_e32 v169, 0xffff0000, v188
	v_pk_fma_f32 v[144:145], v[74:75], v[168:169], v[144:145] op_sel_hi:[0,1,1]
	v_lshlrev_b32_e32 v168, 16, v192
	v_and_b32_e32 v169, 0xffff0000, v192
	v_pk_fma_f32 v[168:169], v[78:79], v[168:169], v[144:145] op_sel_hi:[0,1,1]
	v_pk_add_f32 v[8:9], v[8:9], v[168:169]
	v_pk_add_f32 v[4:5], v[6:7], v[4:5]
	s_waitcnt vmcnt(6)
	v_pk_fma_f32 v[8:9], v[8:9], v[172:173], v[124:125]
	v_pk_mul_f32 v[172:173], v[116:117], v[212:213] op_sel:[1,0] op_sel_hi:[0,1]
	v_lshlrev_b32_e32 v168, 16, v189
	v_and_b32_e32 v169, 0xffff0000, v189
	v_pk_fma_f32 v[172:173], v[116:117], v[214:215], v[172:173]
	v_and_b32_e32 v217, 0xffff0000, v126
	v_pk_fma_f32 v[110:111], v[4:5], v[170:171], v[110:111]
	v_lshlrev_b32_e32 v170, 16, v193
	v_and_b32_e32 v171, 0xffff0000, v193
	v_pk_fma_f32 v[168:169], v[74:75], v[168:169], v[172:173] op_sel_hi:[0,1,1]
	v_lshlrev_b32_e32 v218, 16, v126
	v_pk_fma_f32 v[168:169], v[78:79], v[170:171], v[168:169] op_sel_hi:[0,1,1]
	v_pk_mul_f32 v[172:173], v[116:117], v[216:217] op_sel:[1,0] op_sel_hi:[0,1]
	v_pk_add_f32 v[10:11], v[10:11], v[168:169]
	v_lshlrev_b32_e32 v168, 16, v190
	v_and_b32_e32 v169, 0xffff0000, v190
	v_pk_fma_f32 v[172:173], v[116:117], v[218:219], v[172:173]
	v_lshlrev_b32_e32 v170, 16, v194
	v_and_b32_e32 v171, 0xffff0000, v194
	v_pk_fma_f32 v[168:169], v[74:75], v[168:169], v[172:173] op_sel_hi:[0,1,1]
	v_pk_fma_f32 v[168:169], v[78:79], v[170:171], v[168:169] op_sel_hi:[0,1,1]
	v_pk_mul_f32 v[172:173], v[116:117], v[220:221] op_sel:[1,0] op_sel_hi:[0,1]
	v_pk_add_f32 v[12:13], v[12:13], v[168:169]
	v_lshlrev_b32_e32 v168, 16, v191
	v_and_b32_e32 v169, 0xffff0000, v191
	v_pk_fma_f32 v[172:173], v[116:117], v[228:229], v[172:173]
	v_lshlrev_b32_e32 v170, 16, v195
	v_and_b32_e32 v171, 0xffff0000, v195
	v_pk_fma_f32 v[168:169], v[74:75], v[168:169], v[172:173] op_sel_hi:[0,1,1]
	v_pk_fma_f32 v[168:169], v[78:79], v[170:171], v[168:169] op_sel_hi:[0,1,1]
	v_pk_mul_f32 v[172:173], v[116:117], v[232:233] op_sel:[1,0] op_sel_hi:[0,1]
	v_pk_add_f32 v[14:15], v[14:15], v[168:169]
	v_lshlrev_b32_e32 v168, 16, v150
	v_and_b32_e32 v169, 0xffff0000, v150
	v_pk_fma_f32 v[172:173], v[116:117], v[236:237], v[172:173]
	v_lshlrev_b32_e32 v170, 16, v152
	v_and_b32_e32 v171, 0xffff0000, v152
	v_pk_fma_f32 v[168:169], v[74:75], v[168:169], v[172:173] op_sel_hi:[0,1,1]
	v_and_b32_e32 v241, 0xffff0000, v129
	v_pk_fma_f32 v[168:169], v[78:79], v[170:171], v[168:169] op_sel_hi:[0,1,1]
	v_lshlrev_b32_e32 v242, 16, v129
	v_pk_add_f32 v[16:17], v[16:17], v[168:169]
	v_pk_mul_f32 v[168:169], v[116:117], v[240:241] op_sel:[1,0] op_sel_hi:[0,1]
	v_lshlrev_b32_e32 v150, 16, v151
	v_and_b32_e32 v151, 0xffff0000, v151
	v_pk_fma_f32 v[168:169], v[116:117], v[242:243], v[168:169]
	v_lshlrev_b32_e32 v152, 16, v153
	v_and_b32_e32 v153, 0xffff0000, v153
	v_pk_fma_f32 v[150:151], v[74:75], v[150:151], v[168:169] op_sel_hi:[0,1,1]
	v_pk_fma_f32 v[150:151], v[78:79], v[152:153], v[150:151] op_sel_hi:[0,1,1]
	v_pk_add_f32 v[18:19], v[18:19], v[150:151]
	v_pk_mul_f32 v[158:159], v[116:117], v[158:159] op_sel:[1,0] op_sel_hi:[0,1]
	s_waitcnt vmcnt(4)
; DEVI unsigned cvt_pk(float lo, float hi) { f32x2 v = {lo, hi}; bf16x2_t b = __builtin_convertvector(v, bf16x2_t); return __builtin_bit_cast(unsigned, b); }
; DEVI float bflo(unsigned w) { return __uint_as_float(w << 16); }
; DEVI float bfhi(unsigned w) { return __uint_as_float(w & 0xffff0000u); }
; template <int MODE>
; DEVI void phase_rows(const Params& p, int l, char* smem) {
;     ...
;                 for (int i = 0; i < 8; ++i) {
;                     cacc[i * 4] += f0 * bflo(w0[i][0]) + f1 * bflo(w1[i][0]) + f2 * bflo(w2[i][0]) + f3 * bflo(w3[i][0]);
;                     cacc[i * 4 + 1] += f0 * bfhi(w0[i][0]) + f1 * bfhi(w1[i][0]) + f2 * bfhi(w2[i][0]) + f3 * bfhi(w3[i][0]);
;                     cacc[i * 4 + 2] += f0 * bflo(w0[i][1]) + f1 * bflo(w1[i][1]) + f2 * bflo(w2[i][1]) + f3 * bflo(w3[i][1]);
;                     cacc[i * 4 + 3] += f0 * bfhi(w0[i][1]) + f1 * bfhi(w1[i][1]) + f2 * bfhi(w2[i][1]) + f3 * bfhi(w3[i][1]); }
;             }
;             const float* gf = mrow + 10240;
; #pragma unroll
;             for (int i = 0; i < 8; ++i) { const f32x4 g = *(const f32x4*)(gf + i * 256 + lane * 4);
;                 v[i * 4] += g[0] * cacc[i * 4]; v[i * 4 + 1] += g[1] * cacc[i * 4 + 1]; v[i * 4 + 2] += g[2] * cacc[i * 4 + 2]; v[i * 4 + 3] += g[3] * cacc[i * 4 + 3]; }
;             if (MODE == 2) {
; #pragma unroll
;                 for (int i = 0; i < 8; ++i) *(u32x2*)(xres + (size_t)row * DM + i * 256 + lane * 4) = (u32x2){cvt_pk(v[i * 4], v[i * 4 + 1]), cvt_pk(v[i * 4 + 2], v[i * 4 + 3])};
;             }
;         }
;         f32x4 shv[8], scv[8];
;         if (MODE != 3) { const float* mr2 = (MODE == 2) ? mrow + (size_t)5 * 12288 : mrow;
;             const float* sh = mr2 + ((MODE == 1) ? 6144 : 0); const float* sc = mr2 + ((MODE == 1) ? 8192 : 2048);
; #pragma unroll
;             for (int i = 0; i < 8; ++i) { shv[i] = *(const f32x4*)(sh + i * 256 + lane * 4); scv[i] = *(const f32x4*)(sc + i * 256 + lane * 4); } }
;         float ss = 0.f;
; #pragma unroll
;         for (int i = 0; i < 32; ++i) ss += v[i] * v[i];
	v_pk_fma_f32 v[92:93], v[18:19], v[182:183], v[92:93]
	v_lshlrev_b32_e32 v18, 16, v130
	v_and_b32_e32 v19, 0xffff0000, v130
	v_pk_fma_f32 v[158:159], v[116:117], v[160:161], v[158:159]
	v_lshlrev_b32_e32 v152, 16, v132
	v_and_b32_e32 v153, 0xffff0000, v132
	v_pk_fma_f32 v[18:19], v[74:75], v[18:19], v[158:159] op_sel_hi:[0,1,1]
	v_pk_fma_f32 v[18:19], v[78:79], v[152:153], v[18:19] op_sel_hi:[0,1,1]
	v_pk_add_f32 v[18:19], v[20:21], v[18:19]
	global_load_dwordx4 v[4:7], v[54:55], off
	s_waitcnt vmcnt(4)
	v_pk_fma_f32 v[18:19], v[18:19], v[184:185], v[90:91]
	v_lshlrev_b32_e32 v90, 16, v131
	v_and_b32_e32 v91, 0xffff0000, v131
	v_lshlrev_b32_e32 v130, 16, v133
	v_and_b32_e32 v131, 0xffff0000, v133
	v_pk_mul_f32 v[132:133], v[116:117], v[154:155] op_sel:[1,0] op_sel_hi:[0,1]
	v_pk_fma_f32 v[132:133], v[116:117], v[156:157], v[132:133]
	v_lshlrev_b32_e32 v134, 16, v138
	v_and_b32_e32 v137, 0xffff0000, v138
	v_lshlrev_b32_e32 v126, 16, v139
	v_and_b32_e32 v129, 0xffff0000, v139
	v_pk_mul_f32 v[138:139], v[100:101], v[100:101]
	v_pk_fma_f32 v[90:91], v[74:75], v[90:91], v[132:133] op_sel_hi:[0,1,1]
	v_pk_mul_f32 v[144:145], v[110:111], v[110:111]
	v_pk_fma_f32 v[90:91], v[78:79], v[130:131], v[90:91] op_sel_hi:[0,1,1]
	v_pk_mul_f32 v[132:133], v[116:117], v[146:147] op_sel:[1,0] op_sel_hi:[0,1]
	v_add_f32_e32 v1, v138, v139
	v_pk_add_f32 v[22:23], v[22:23], v[90:91]
	v_lshlrev_b32_e32 v90, 16, v112
	v_and_b32_e32 v91, 0xffff0000, v112
	v_pk_fma_f32 v[132:133], v[116:117], v[148:149], v[132:133]
	v_add_f32_e32 v1, v144, v1
	v_pk_mul_f32 v[124:125], v[8:9], v[8:9]
	v_lshlrev_b32_e32 v130, 16, v114
	v_and_b32_e32 v131, 0xffff0000, v114
	v_pk_fma_f32 v[90:91], v[74:75], v[90:91], v[132:133] op_sel_hi:[0,1,1]
	v_add_f32_e32 v1, v145, v1
	v_pk_fma_f32 v[10:11], v[10:11], v[174:175], v[118:119]
	v_pk_fma_f32 v[90:91], v[78:79], v[130:131], v[90:91] op_sel_hi:[0,1,1]
	v_add_f32_e32 v1, v124, v1
	v_pk_mul_f32 v[118:119], v[10:11], v[10:11]
	v_pk_add_f32 v[24:25], v[24:25], v[90:91]
	v_add_f32_e32 v1, v125, v1
	v_pk_fma_f32 v[12:13], v[12:13], v[176:177], v[104:105]
	s_waitcnt vmcnt(3)
	v_pk_fma_f32 v[24:25], v[24:25], v[44:45], v[86:87]
	v_lshlrev_b32_e32 v86, 16, v113
	v_and_b32_e32 v87, 0xffff0000, v113
	v_pk_mul_f32 v[112:113], v[116:117], v[140:141] op_sel:[1,0] op_sel_hi:[0,1]
	v_add_f32_e32 v1, v118, v1
	v_pk_mul_f32 v[104:105], v[12:13], v[12:13]
	v_pk_fma_f32 v[112:113], v[116:117], v[142:143], v[112:113]
	v_add_f32_e32 v1, v119, v1
	v_pk_fma_f32 v[14:15], v[14:15], v[178:179], v[102:103]
	v_lshlrev_b32_e32 v90, 16, v115
	v_and_b32_e32 v91, 0xffff0000, v115
	v_pk_fma_f32 v[86:87], v[74:75], v[86:87], v[112:113] op_sel_hi:[0,1,1]
	v_add_f32_e32 v1, v104, v1
	v_pk_mul_f32 v[102:103], v[14:15], v[14:15]
	v_pk_fma_f32 v[86:87], v[78:79], v[90:91], v[86:87] op_sel_hi:[0,1,1]
	v_add_f32_e32 v1, v105, v1
	v_pk_fma_f32 v[16:17], v[16:17], v[180:181], v[94:95]
	v_pk_add_f32 v[26:27], v[26:27], v[86:87]
	v_pk_mul_f32 v[90:91], v[116:117], v[134:135] op_sel:[1,0] op_sel_hi:[0,1]
	v_add_f32_e32 v1, v102, v1
	v_pk_mul_f32 v[94:95], v[16:17], v[16:17]
	v_pk_fma_f32 v[26:27], v[26:27], v[46:47], v[84:85]
	v_lshlrev_b32_e32 v84, 16, v96
	v_and_b32_e32 v85, 0xffff0000, v96
	v_pk_fma_f32 v[90:91], v[116:117], v[136:137], v[90:91]
	v_add_f32_e32 v1, v103, v1
	v_lshlrev_b32_e32 v86, 16, v98
	v_and_b32_e32 v87, 0xffff0000, v98
	v_pk_fma_f32 v[84:85], v[74:75], v[84:85], v[90:91] op_sel_hi:[0,1,1]
	v_add_f32_e32 v1, v94, v1
	v_pk_mul_f32 v[150:151], v[92:93], v[92:93]
	v_pk_fma_f32 v[84:85], v[78:79], v[86:87], v[84:85] op_sel_hi:[0,1,1]
	v_add_f32_e32 v1, v95, v1
	v_pk_add_f32 v[28:29], v[28:29], v[84:85]
	v_pk_mul_f32 v[86:87], v[116:117], v[126:127] op_sel:[1,0] op_sel_hi:[0,1]
	v_add_f32_e32 v1, v150, v1
	v_pk_mul_f32 v[20:21], v[18:19], v[18:19]
	s_waitcnt vmcnt(2)
	v_pk_fma_f32 v[28:29], v[28:29], v[40:41], v[82:83]
	v_lshlrev_b32_e32 v82, 16, v97
	v_and_b32_e32 v83, 0xffff0000, v97
	v_pk_fma_f32 v[86:87], v[116:117], v[128:129], v[86:87]
	v_add_f32_e32 v1, v151, v1
	v_pk_fma_f32 v[22:23], v[22:23], v[186:187], v[88:89]
	v_lshlrev_b32_e32 v84, 16, v99
	v_and_b32_e32 v85, 0xffff0000, v99
	v_pk_fma_f32 v[82:83], v[74:75], v[82:83], v[86:87] op_sel_hi:[0,1,1]
	v_add_f32_e32 v1, v20, v1
	v_pk_mul_f32 v[88:89], v[22:23], v[22:23]
	v_pk_fma_f32 v[82:83], v[78:79], v[84:85], v[82:83] op_sel_hi:[0,1,1]
	v_add_f32_e32 v1, v21, v1
	v_pk_add_f32 v[30:31], v[30:31], v[82:83]
	v_pk_mul_f32 v[84:85], v[116:117], v[120:121] op_sel:[1,0] op_sel_hi:[0,1]
	v_add_f32_e32 v1, v88, v1
	v_pk_mul_f32 v[44:45], v[24:25], v[24:25]
	v_pk_fma_f32 v[30:31], v[30:31], v[42:43], v[80:81]
	v_lshlrev_b32_e32 v80, 16, v72
	v_and_b32_e32 v81, 0xffff0000, v72
	v_pk_fma_f32 v[84:85], v[116:117], v[122:123], v[84:85]
	v_add_f32_e32 v1, v89, v1
	v_lshlrev_b32_e32 v82, 16, v76
	v_and_b32_e32 v83, 0xffff0000, v76
	v_pk_fma_f32 v[80:81], v[74:75], v[80:81], v[84:85] op_sel_hi:[0,1,1]
	v_add_f32_e32 v1, v44, v1
	v_pk_mul_f32 v[46:47], v[26:27], v[26:27]
	v_pk_fma_f32 v[80:81], v[78:79], v[82:83], v[80:81] op_sel_hi:[0,1,1]
	v_add_f32_e32 v1, v45, v1
	v_pk_add_f32 v[32:33], v[32:33], v[80:81]
	v_add_f32_e32 v1, v46, v1
	v_pk_mul_f32 v[40:41], v[28:29], v[28:29]
	s_waitcnt vmcnt(1)
; template <int MODE>
; DEVI void phase_rows(const Params& p, int l, char* smem) {
;     ...
;         ss = wave_sum(ss);
;         const float rstd = rsqrtf(ss * (1.f / DM) + EPS);
;         if (MODE == 3) {
; #pragma unroll
;             for (int i = 0; i < 8; ++i) { const f32x4 g = *(const f32x4*)(p.final_norm + i * 256 + lane * 4);
;                 __builtin_nontemporal_store((f32x4){v[i * 4] * rstd * g[0], v[i * 4 + 1] * rstd * g[1], v[i * 4 + 2] * rstd * g[2], v[i * 4 + 3] * rstd * g[3]}, (f32x4*)(p.out + (size_t)row * DM + i * 256 + lane * 4)); }
;             continue;
	v_pk_fma_f32 v[32:33], v[32:33], v[36:37], v[70:71]
	v_lshlrev_b32_e32 v70, 16, v73
	v_and_b32_e32 v71, 0xffff0000, v73
	v_lshlrev_b32_e32 v72, 16, v77
	v_and_b32_e32 v73, 0xffff0000, v77
	v_pk_mul_f32 v[76:77], v[116:117], v[106:107] op_sel:[1,0] op_sel_hi:[0,1]
	v_add_f32_e32 v1, v47, v1
	v_pk_fma_f32 v[76:77], v[116:117], v[108:109], v[76:77]
	v_add_f32_e32 v1, v40, v1
	v_pk_mul_f32 v[42:43], v[30:31], v[30:31]
	v_pk_fma_f32 v[70:71], v[74:75], v[70:71], v[76:77] op_sel_hi:[0,1,1]
	v_add_f32_e32 v1, v41, v1
	v_pk_fma_f32 v[70:71], v[78:79], v[72:73], v[70:71] op_sel_hi:[0,1,1]
	v_add_f32_e32 v1, v42, v1
	v_pk_mul_f32 v[36:37], v[32:33], v[32:33]
	v_pk_add_f32 v[34:35], v[34:35], v[70:71]
	v_add_f32_e32 v1, v43, v1
	v_pk_fma_f32 v[34:35], v[34:35], v[38:39], v[68:69]
	v_add_f32_e32 v1, v36, v1
	v_pk_mul_f32 v[38:39], v[34:35], v[34:35]
	v_add_f32_e32 v1, v37, v1
	v_add_f32_e32 v1, v38, v1
	v_add_f32_e32 v1, v39, v1
	ds_bpermute_b32 v20, v51, v1
	s_waitcnt lgkmcnt(0)
	v_add_f32_e32 v1, v1, v20
	ds_bpermute_b32 v20, v162, v1
	s_waitcnt lgkmcnt(0)
	v_add_f32_e32 v1, v1, v20
	ds_bpermute_b32 v20, v163, v1
	s_waitcnt lgkmcnt(0)
	v_add_f32_e32 v1, v1, v20
	ds_bpermute_b32 v20, v164, v1
	s_waitcnt lgkmcnt(0)
	v_add_f32_e32 v1, v1, v20
	ds_bpermute_b32 v20, v165, v1
	s_waitcnt lgkmcnt(0)
	v_add_f32_e32 v1, v1, v20
	ds_bpermute_b32 v20, v166, v1
	s_waitcnt lgkmcnt(0)
	v_add_f32_e32 v1, v1, v20
	v_fmamk_f32 v1, v1, 0x3a000000, v223
	v_mul_f32_e32 v20, 0x4b800000, v1
	v_cmp_gt_f32_e32 vcc, s97, v1
	s_nop 1
	v_cndmask_b32_e32 v1, v1, v20, vcc
	v_rsq_f32_e32 v1, v1
	v_lshlrev_b64 v[20:21], 2, v[66:67]
	v_lshl_add_u64 v[36:37], v[56:57], 0, v[20:21]
	v_mul_f32_e32 v38, 0x45800000, v1
	v_cndmask_b32_e32 v38, v1, v38, vcc
	v_pk_mul_f32 v[40:41], v[100:101], v[38:39] op_sel_hi:[1,0]
	v_pk_mul_f32 v[42:43], v[110:111], v[38:39] op_sel_hi:[1,0]
	global_load_dwordx4 v[198:201], v[54:55], off offset:1024
	global_load_dwordx4 v[202:205], v[54:55], off offset:2048
	global_load_dwordx4 v[206:209], v[54:55], off offset:3072
	global_load_dwordx4 v[210:213], v[58:59], off
	global_load_dwordx4 v[214:217], v[60:61], off
	global_load_dwordx4 v[218:221], v[62:63], off
	global_load_dwordx4 v[168:171], v[64:65], off
	s_waitcnt vmcnt(0)
	v_pk_mul_f32 v[4:5], v[4:5], v[40:41]
	v_pk_mul_f32 v[6:7], v[6:7], v[42:43]
	global_store_dwordx4 v[36:37], v[4:7], off nt
	s_load_dwordx4 s[4:7], s[0:1], 0x90
	v_pk_mul_f32 v[10:11], v[10:11], v[38:39] op_sel_hi:[1,0]
	v_pk_mul_f32 v[8:9], v[8:9], v[38:39] op_sel_hi:[1,0]
	s_waitcnt lgkmcnt(0)
	s_movk_i32 s4, 0x1000
	v_lshl_add_u64 v[20:21], s[6:7], 0, v[20:21]
	v_lshl_add_u64 v[20:21], v[20:21], 0, v[2:3]
	v_pk_mul_f32 v[4:5], v[198:199], v[8:9]
	v_pk_mul_f32 v[6:7], v[200:201], v[10:11]
	global_store_dwordx4 v[20:21], v[4:7], off offset:1024 nt
	v_pk_mul_f32 v[8:9], v[14:15], v[38:39] op_sel_hi:[1,0]
	v_pk_mul_f32 v[10:11], v[12:13], v[38:39] op_sel_hi:[1,0]
	v_pk_mul_f32 v[12:13], v[18:19], v[38:39] op_sel_hi:[1,0]
	v_pk_mul_f32 v[4:5], v[202:203], v[10:11]
	v_pk_mul_f32 v[6:7], v[204:205], v[8:9]
	global_store_dwordx4 v[20:21], v[4:7], off offset:2048 nt
	v_pk_mul_f32 v[8:9], v[92:93], v[38:39] op_sel_hi:[1,0]
	v_pk_mul_f32 v[10:11], v[16:17], v[38:39] op_sel_hi:[1,0]
	v_pk_mul_f32 v[6:7], v[208:209], v[8:9]
	v_pk_mul_f32 v[4:5], v[206:207], v[10:11]
	global_store_dwordx4 v[20:21], v[4:7], off offset:3072 nt
	v_add_co_u32_e32 v8, vcc, s4, v20
	v_pk_mul_f32 v[10:11], v[22:23], v[38:39] op_sel_hi:[1,0]
	s_nop 0
	v_addc_co_u32_e32 v9, vcc, 0, v21, vcc
	v_cmp_lt_i32_e32 vcc, s73, v48
	s_or_b64 s[42:43], vcc, s[42:43]
	v_pk_mul_f32 v[4:5], v[210:211], v[12:13]
	v_pk_mul_f32 v[6:7], v[212:213], v[10:11]
	global_store_dwordx4 v[8:9], v[4:7], off nt
	v_pk_mul_f32 v[10:11], v[26:27], v[38:39] op_sel_hi:[1,0]
	v_pk_mul_f32 v[12:13], v[24:25], v[38:39] op_sel_hi:[1,0]
	v_pk_mul_f32 v[6:7], v[216:217], v[10:11]
	v_pk_mul_f32 v[4:5], v[214:215], v[12:13]
	global_store_dwordx4 v[8:9], v[4:7], off offset:1024 nt
	v_pk_mul_f32 v[10:11], v[30:31], v[38:39] op_sel_hi:[1,0]
	v_pk_mul_f32 v[12:13], v[28:29], v[38:39] op_sel_hi:[1,0]
	v_pk_mul_f32 v[6:7], v[220:221], v[10:11]
	v_pk_mul_f32 v[4:5], v[218:219], v[12:13]
	global_store_dwordx4 v[8:9], v[4:7], off offset:2048 nt
	v_pk_mul_f32 v[10:11], v[34:35], v[38:39] op_sel_hi:[1,0]
	v_pk_mul_f32 v[12:13], v[32:33], v[38:39] op_sel_hi:[1,0]
	v_pk_mul_f32 v[6:7], v[170:171], v[10:11]
	v_pk_mul_f32 v[4:5], v[168:169], v[12:13]
	global_store_dwordx4 v[8:9], v[4:7], off offset:3072 nt
	s_andn2_b64 exec, exec, s[42:43]
	s_cbranch_execz .LBB0_1896
